# FFN-norm/router phase: all row loads of the rstd pass issued up front into spare registers (copied into place where the late loads used to be issued) so the two HBM round trips overlap
# speedup vs baseline: 1.0122x; 1.0052x over previous
; __device__ __forceinline__ float bf_lo(unsigned w) { return __uint_as_float(w << 16); }
; __device__ __forceinline__ float bf_hi(unsigned w) { return __uint_as_float(w & 0xffff0000u); }
; __device__ __forceinline__ void phase_nrr(const Frame& F, const Args& a, int l, const bf16_t* XA, const float* g, const float* modl, unsigned char* XN8) {
;     ...
;         const int tb = tile * 64 + w * 8, b = tb / S;
;         __syncthreads();
;         if (F.tid < NE) hist[F.tid] = 0;
;         float rs[8];
; #pragma unroll
;         for (int i4 = 0; i4 < 2; ++i4) { u32x4 rw[4][4];
; #pragma unroll
;             for (int i = 0; i < 4; ++i)
; #pragma unroll
;                 for (int j = 0; j < 4; ++j) rw[i][j] = *(const u32x4*)(XA + (size_t)(tb + 4 * i4 + i) * D + (j * 64 + lane) * 8);
; #pragma unroll
;             for (int i = 0; i < 4; ++i) { float ss = 0.f;
; #pragma unroll
;                 for (int j = 0; j < 4; ++j)
; #pragma unroll
;                     for (int q = 0; q < 4; ++q) { const float x0 = bf_lo(rw[i][j][q]), x1 = bf_hi(rw[i][j][q]); ss += x0 * x0; ss += x1 * x1; }
;                 rs[4 * i4 + i] = rsqrtf(wave_sum(ss) * (1.f / D) + EPS); } }
.LBB0_527:
	s_waitcnt vmcnt(0)
	s_barrier
	s_and_saveexec_b64 s[2:3], s[20:21]
	ds_write_b32 v241, v195
	s_or_b64 exec, exec, s[2:3]
	s_lshl_b32 s91, s90, 6
	s_add_i32 s44, s91, s72
	s_ashr_i32 s45, s44, 31
	s_lshl_b64 s[2:3], s[44:45], 12
	v_lshl_add_u64 v[204:205], v[202:203], 0, s[2:3]
	s_or_b32 s42, s44, 1
	global_load_dwordx4 v[2:5], v[204:205], off offset:1024
	global_load_dwordx4 v[38:41], v[204:205], off offset:2048
	global_load_dwordx4 v[46:49], v[204:205], off offset:3072
	global_load_dwordx4 v[6:9], v[204:205], off
	s_ashr_i32 s43, s42, 31
	s_lshl_b64 s[2:3], s[42:43], 12
	v_lshl_add_u64 v[206:207], v[202:203], 0, s[2:3]
	global_load_dwordx4 v[10:13], v[206:207], off
	global_load_dwordx4 v[14:17], v[206:207], off offset:1024
	global_load_dwordx4 v[50:53], v[206:207], off offset:2048
	global_load_dwordx4 v[54:57], v[206:207], off offset:3072
	s_or_b32 s40, s44, 2
	s_or_b32 s4, s44, 3
	s_ashr_i32 s41, s40, 31
	s_ashr_i32 s5, s4, 31
	s_lshl_b64 s[2:3], s[40:41], 12
	s_lshl_b64 s[22:23], s[4:5], 12
	v_lshl_add_u64 v[208:209], v[202:203], 0, s[2:3]
	v_lshl_add_u64 v[210:211], v[202:203], 0, s[22:23]
	global_load_dwordx4 v[18:21], v[208:209], off
	global_load_dwordx4 v[22:25], v[208:209], off offset:1024
	global_load_dwordx4 v[34:37], v[208:209], off offset:2048
	global_load_dwordx4 v[42:45], v[208:209], off offset:3072
	global_load_dwordx4 v[26:29], v[210:211], off
	global_load_dwordx4 v[30:33], v[210:211], off offset:1024
	s_or_b32 s2, s44, 4
	s_ashr_i32 s3, s2, 31
	s_or_b32 s56, s44, 5
	s_lshl_b64 s[22:23], s[2:3], 12
	s_ashr_i32 s57, s56, 31
	v_lshl_add_u64 v[212:213], v[202:203], 0, s[22:23]
	s_lshl_b64 s[22:23], s[56:57], 12
	v_lshl_add_u64 v[214:215], v[202:203], 0, s[22:23]
	s_mov_b32 s22, 0x358637bd
	s_or_b32 s58, s44, 6
	s_ashr_i32 s59, s58, 31
	s_or_b32 s60, s44, 7
	s_lshl_b64 s[24:25], s[58:59], 12
	s_ashr_i32 s61, s60, 31
	v_lshl_add_u64 v[216:217], v[202:203], 0, s[24:25]
	s_lshl_b64 s[24:25], s[60:61], 12
	v_lshl_add_u64 v[218:219], v[202:203], 0, s[24:25]
	s_mov_b64 s[62:63], -1
	s_mov_b64 s[66:67], 0
	global_load_dwordx4 v[134:137], v[210:211], off offset:2048
	global_load_dwordx4 v[138:141], v[210:211], off offset:3072
	global_load_dwordx4 v[142:145], v[212:213], off
	global_load_dwordx4 v[146:149], v[212:213], off offset:1024
	global_load_dwordx4 v[150:153], v[212:213], off offset:2048
	global_load_dwordx4 v[154:157], v[212:213], off offset:3072
	global_load_dwordx4 v[158:161], v[214:215], off
	global_load_dwordx4 v[162:165], v[214:215], off offset:2048
	global_load_dwordx4 v[166:169], v[214:215], off offset:3072
	global_load_dwordx4 v[170:173], v[214:215], off offset:1024
	global_load_dwordx4 v[174:177], v[216:217], off
	global_load_dwordx4 v[178:181], v[216:217], off offset:1024
	global_load_dwordx4 v[182:185], v[216:217], off offset:2048
	global_load_dwordx4 v[186:189], v[216:217], off offset:3072
	global_load_dwordx4 v[190:193], v[218:219], off
	global_load_dwordx4 v[114:117], v[218:219], off offset:1024
	global_load_dwordx4 v[118:121], v[218:219], off offset:2048
	global_load_dwordx4 v[126:129], v[218:219], off offset:3072
	s_waitcnt vmcnt(31)
	v_lshlrev_b32_e32 v81, 16, v2
	v_and_b32_e32 v59, 0xffff0000, v2
	v_lshlrev_b32_e32 v83, 16, v3
	s_waitcnt vmcnt(28)
	v_lshlrev_b32_e32 v65, 16, v6
	s_waitcnt vmcnt(27)
	v_lshlrev_b32_e32 v64, 16, v10
	v_and_b32_e32 v67, 0xffff0000, v6
	v_and_b32_e32 v66, 0xffff0000, v10
	v_pk_mul_f32 v[64:65], v[64:65], v[64:65]
	v_lshlrev_b32_e32 v69, 16, v7
	v_lshlrev_b32_e32 v68, 16, v11
	v_pk_fma_f32 v[64:65], v[66:67], v[66:67], v[64:65]
	v_and_b32_e32 v71, 0xffff0000, v7
	v_and_b32_e32 v70, 0xffff0000, v11
	v_pk_fma_f32 v[64:65], v[68:69], v[68:69], v[64:65]
	v_lshlrev_b32_e32 v73, 16, v8
	v_lshlrev_b32_e32 v72, 16, v12
	v_pk_fma_f32 v[64:65], v[70:71], v[70:71], v[64:65]
	v_and_b32_e32 v75, 0xffff0000, v8
	v_and_b32_e32 v74, 0xffff0000, v12
	v_pk_fma_f32 v[64:65], v[72:73], v[72:73], v[64:65]
	v_lshlrev_b32_e32 v77, 16, v9
	v_lshlrev_b32_e32 v76, 16, v13
	v_pk_fma_f32 v[64:65], v[74:75], v[74:75], v[64:65]
	v_and_b32_e32 v79, 0xffff0000, v9
	v_and_b32_e32 v78, 0xffff0000, v13
	v_pk_fma_f32 v[64:65], v[76:77], v[76:77], v[64:65]
	s_waitcnt vmcnt(26)
	v_lshlrev_b32_e32 v80, 16, v14
	v_pk_fma_f32 v[64:65], v[78:79], v[78:79], v[64:65]
	v_and_b32_e32 v58, 0xffff0000, v14
	v_pk_fma_f32 v[64:65], v[80:81], v[80:81], v[64:65]
	v_lshlrev_b32_e32 v82, 16, v15
	v_pk_fma_f32 v[58:59], v[58:59], v[58:59], v[64:65]
	v_and_b32_e32 v85, 0xffff0000, v3
	v_and_b32_e32 v84, 0xffff0000, v15
	v_pk_fma_f32 v[58:59], v[82:83], v[82:83], v[58:59]
	v_lshlrev_b32_e32 v87, 16, v4
	v_lshlrev_b32_e32 v86, 16, v16
	v_pk_fma_f32 v[58:59], v[84:85], v[84:85], v[58:59]
	v_and_b32_e32 v89, 0xffff0000, v4
	v_and_b32_e32 v88, 0xffff0000, v16
	v_pk_fma_f32 v[58:59], v[86:87], v[86:87], v[58:59]
	v_lshlrev_b32_e32 v91, 16, v5
	v_lshlrev_b32_e32 v90, 16, v17
	v_pk_fma_f32 v[58:59], v[88:89], v[88:89], v[58:59]
	v_and_b32_e32 v93, 0xffff0000, v5
	v_and_b32_e32 v92, 0xffff0000, v17
	v_pk_fma_f32 v[58:59], v[90:91], v[90:91], v[58:59]
	v_lshlrev_b32_e32 v95, 16, v38
	s_waitcnt vmcnt(25)
; __device__ __forceinline__ float bf_lo(unsigned w) { return __uint_as_float(w << 16); }
; __device__ __forceinline__ float bf_hi(unsigned w) { return __uint_as_float(w & 0xffff0000u); }
; __device__ __forceinline__ void phase_nrr(const Frame& F, const Args& a, int l, const bf16_t* XA, const float* g, const float* modl, unsigned char* XN8) {
;     ...
;         const int tb = tile * 64 + w * 8, b = tb / S;
;         __syncthreads();
;         if (F.tid < NE) hist[F.tid] = 0;
;         float rs[8];
; #pragma unroll
;         for (int i4 = 0; i4 < 2; ++i4) { u32x4 rw[4][4];
; #pragma unroll
;             for (int i = 0; i < 4; ++i)
; #pragma unroll
;                 for (int j = 0; j < 4; ++j) rw[i][j] = *(const u32x4*)(XA + (size_t)(tb + 4 * i4 + i) * D + (j * 64 + lane) * 8);
; #pragma unroll
;             for (int i = 0; i < 4; ++i) { float ss = 0.f;
; #pragma unroll
;                 for (int j = 0; j < 4; ++j)
; #pragma unroll
;                     for (int q = 0; q < 4; ++q) { const float x0 = bf_lo(rw[i][j][q]), x1 = bf_hi(rw[i][j][q]); ss += x0 * x0; ss += x1 * x1; }
;                 rs[4 * i4 + i] = rsqrtf(wave_sum(ss) * (1.f / D) + EPS); } }
	v_lshlrev_b32_e32 v94, 16, v50
	v_pk_fma_f32 v[58:59], v[92:93], v[92:93], v[58:59]
	v_and_b32_e32 v97, 0xffff0000, v38
	v_and_b32_e32 v96, 0xffff0000, v50
	v_pk_fma_f32 v[58:59], v[94:95], v[94:95], v[58:59]
	v_and_b32_e32 v99, 0xffff0000, v39
	v_lshlrev_b32_e32 v39, 16, v39
	v_lshlrev_b32_e32 v38, 16, v51
	v_pk_fma_f32 v[58:59], v[96:97], v[96:97], v[58:59]
	v_and_b32_e32 v98, 0xffff0000, v51
	v_pk_fma_f32 v[38:39], v[38:39], v[38:39], v[58:59]
	v_lshlrev_b32_e32 v61, 16, v40
	v_lshlrev_b32_e32 v60, 16, v52
	v_pk_fma_f32 v[38:39], v[98:99], v[98:99], v[38:39]
	v_and_b32_e32 v101, 0xffff0000, v40
	v_and_b32_e32 v100, 0xffff0000, v52
	v_pk_fma_f32 v[38:39], v[60:61], v[60:61], v[38:39]
	v_lshlrev_b32_e32 v103, 16, v41
	v_lshlrev_b32_e32 v102, 16, v53
	v_pk_fma_f32 v[38:39], v[100:101], v[100:101], v[38:39]
	v_and_b32_e32 v41, 0xffff0000, v41
	v_and_b32_e32 v40, 0xffff0000, v53
	v_pk_fma_f32 v[38:39], v[102:103], v[102:103], v[38:39]
	v_and_b32_e32 v53, 0xffff0000, v46
	v_pk_fma_f32 v[38:39], v[40:41], v[40:41], v[38:39]
	v_lshlrev_b32_e32 v41, 16, v46
	s_waitcnt vmcnt(24)
	v_lshlrev_b32_e32 v40, 16, v54
	v_and_b32_e32 v52, 0xffff0000, v54
	v_pk_fma_f32 v[38:39], v[40:41], v[40:41], v[38:39]
	v_and_b32_e32 v62, 0xffff0000, v48
	v_lshlrev_b32_e32 v63, 16, v48
	v_and_b32_e32 v50, 0xffff0000, v56
	v_lshlrev_b32_e32 v51, 16, v56
	v_pk_fma_f32 v[38:39], v[52:53], v[52:53], v[38:39]
	v_lshlrev_b32_e32 v41, 16, v47
	v_lshlrev_b32_e32 v40, 16, v55
	v_pk_mul_f32 v[62:63], v[62:63], v[62:63]
	v_pk_mul_f32 v[50:51], v[50:51], v[50:51]
	v_and_b32_e32 v47, 0xffff0000, v47
	v_and_b32_e32 v46, 0xffff0000, v55
	v_pk_fma_f32 v[38:39], v[40:41], v[40:41], v[38:39]
	v_mov_b32_e32 v40, v51
	v_pk_fma_f32 v[38:39], v[46:47], v[46:47], v[38:39]
	v_mov_b32_e32 v41, v63
	v_and_b32_e32 v48, 0xffff0000, v49
	v_lshlrev_b32_e32 v49, 16, v49
	v_pk_add_f32 v[38:39], v[40:41], v[38:39]
	v_and_b32_e32 v40, 0xffff0000, v57
	v_lshlrev_b32_e32 v41, 16, v57
	v_pk_mul_f32 v[48:49], v[48:49], v[48:49]
	v_pk_mul_f32 v[40:41], v[40:41], v[40:41]
	v_mov_b32_e32 v51, v62
	v_pk_add_f32 v[38:39], v[50:51], v[38:39]
	v_mov_b32_e32 v46, v41
	v_mov_b32_e32 v47, v49
	v_pk_add_f32 v[38:39], v[46:47], v[38:39]
	v_mov_b32_e32 v41, v48
	v_pk_add_f32 v[46:47], v[40:41], v[38:39]
	ds_bpermute_b32 v49, v1, v47
	ds_bpermute_b32 v48, v1, v46
	s_waitcnt vmcnt(17)
	v_mov_b64_e32 v[38:39], v[134:135]
	v_mov_b64_e32 v[40:41], v[136:137]
	s_waitcnt vmcnt(17)
	v_and_b32_e32 v58, 0xffff0000, v44
	v_lshlrev_b32_e32 v59, 16, v44
	v_and_b32_e32 v44, 0xffff0000, v45
	s_waitcnt lgkmcnt(0)
	v_pk_add_f32 v[46:47], v[46:47], v[48:49]
	ds_bpermute_b32 v49, v201, v47
	ds_bpermute_b32 v48, v201, v46
	v_lshlrev_b32_e32 v45, 16, v45
	v_pk_mul_f32 v[60:61], v[44:45], v[44:45]
	v_lshlrev_b32_e32 v45, 16, v18
	s_waitcnt vmcnt(17)
	v_lshlrev_b32_e32 v44, 16, v26
	s_waitcnt lgkmcnt(0)
	v_pk_add_f32 v[50:51], v[46:47], v[48:49]
	s_waitcnt vmcnt(16)
	v_mov_b64_e32 v[46:47], v[138:139]
	v_mov_b64_e32 v[48:49], v[140:141]
	v_and_b32_e32 v63, 0xffff0000, v18
	v_and_b32_e32 v62, 0xffff0000, v26
	v_pk_mul_f32 v[44:45], v[44:45], v[44:45]
	v_and_b32_e32 v65, 0xffff0000, v19
	v_pk_fma_f32 v[44:45], v[62:63], v[62:63], v[44:45]
	v_lshlrev_b32_e32 v63, 16, v19
	v_lshlrev_b32_e32 v62, 16, v27
	v_and_b32_e32 v64, 0xffff0000, v27
	v_pk_fma_f32 v[44:45], v[62:63], v[62:63], v[44:45]
	v_lshlrev_b32_e32 v63, 16, v20
	v_pk_fma_f32 v[44:45], v[64:65], v[64:65], v[44:45]
	v_lshlrev_b32_e32 v62, 16, v28
	v_and_b32_e32 v65, 0xffff0000, v20
	v_and_b32_e32 v64, 0xffff0000, v28
	v_pk_fma_f32 v[44:45], v[62:63], v[62:63], v[44:45]
	v_lshlrev_b32_e32 v63, 16, v21
	v_pk_fma_f32 v[44:45], v[64:65], v[64:65], v[44:45]
	v_lshlrev_b32_e32 v62, 16, v29
	v_pk_fma_f32 v[44:45], v[62:63], v[62:63], v[44:45]
	v_and_b32_e32 v63, 0xffff0000, v21
	v_and_b32_e32 v62, 0xffff0000, v29
	v_lshlrev_b32_e32 v65, 16, v22
	s_waitcnt vmcnt(16)
	v_lshlrev_b32_e32 v64, 16, v30
	v_pk_fma_f32 v[44:45], v[62:63], v[62:63], v[44:45]
	v_and_b32_e32 v55, 0xffff0000, v22
	v_and_b32_e32 v54, 0xffff0000, v30
	v_pk_fma_f32 v[44:45], v[64:65], v[64:65], v[44:45]
	v_and_b32_e32 v63, 0xffff0000, v23
	v_pk_fma_f32 v[44:45], v[54:55], v[54:55], v[44:45]
	v_lshlrev_b32_e32 v55, 16, v23
	v_lshlrev_b32_e32 v54, 16, v31
	v_and_b32_e32 v62, 0xffff0000, v31
	v_pk_fma_f32 v[44:45], v[54:55], v[54:55], v[44:45]
	v_lshlrev_b32_e32 v55, 16, v24
	v_pk_fma_f32 v[44:45], v[62:63], v[62:63], v[44:45]
	v_lshlrev_b32_e32 v54, 16, v32
	v_and_b32_e32 v63, 0xffff0000, v24
	v_and_b32_e32 v62, 0xffff0000, v32
	v_pk_fma_f32 v[44:45], v[54:55], v[54:55], v[44:45]
	v_lshlrev_b32_e32 v55, 16, v25
	v_pk_fma_f32 v[44:45], v[62:63], v[62:63], v[44:45]
	v_lshlrev_b32_e32 v54, 16, v33
	v_and_b32_e32 v63, 0xffff0000, v25
	v_and_b32_e32 v62, 0xffff0000, v33
	v_pk_fma_f32 v[44:45], v[54:55], v[54:55], v[44:45]
	v_lshlrev_b32_e32 v55, 16, v34
	v_pk_fma_f32 v[44:45], v[62:63], v[62:63], v[44:45]
	v_and_b32_e32 v63, 0xffff0000, v34
	v_lshlrev_b32_e32 v57, 16, v36
	v_pk_mul_f32 v[58:59], v[58:59], v[58:59]
	v_and_b32_e32 v65, 0xffff0000, v43
	ds_bpermute_b32 v53, v220, v51
	ds_bpermute_b32 v52, v220, v50
	v_mov_b64_e32 v[78:79], s[22:23]
	s_lshr_b32 s22, s45, 20
	s_add_i32 s22, s44, s22
	s_ashr_i32 s36, s22, 12
	s_waitcnt lgkmcnt(0)
	v_pk_add_f32 v[50:51], v[50:51], v[52:53]
	ds_bpermute_b32 v53, v221, v51
	ds_bpermute_b32 v52, v221, v50
	s_waitcnt lgkmcnt(0)
	v_pk_add_f32 v[50:51], v[50:51], v[52:53]
	ds_bpermute_b32 v53, v222, v51
	ds_bpermute_b32 v52, v222, v50
	s_waitcnt vmcnt(16)
; __device__ __forceinline__ float bf_lo(unsigned w) { return __uint_as_float(w << 16); }
; __device__ __forceinline__ float bf_hi(unsigned w) { return __uint_as_float(w & 0xffff0000u); }
; __device__ __forceinline__ void phase_nrr(const Frame& F, const Args& a, int l, const bf16_t* XA, const float* g, const float* modl, unsigned char* XN8) {
;     ...
;         const int tb = tile * 64 + w * 8, b = tb / S;
;         __syncthreads();
;         if (F.tid < NE) hist[F.tid] = 0;
;         float rs[8];
; #pragma unroll
;         for (int i4 = 0; i4 < 2; ++i4) { u32x4 rw[4][4];
; #pragma unroll
;             for (int i = 0; i < 4; ++i)
; #pragma unroll
;                 for (int j = 0; j < 4; ++j) rw[i][j] = *(const u32x4*)(XA + (size_t)(tb + 4 * i4 + i) * D + (j * 64 + lane) * 8);
; #pragma unroll
;             for (int i = 0; i < 4; ++i) { float ss = 0.f;
; #pragma unroll
;                 for (int j = 0; j < 4; ++j)
; #pragma unroll
;                     for (int q = 0; q < 4; ++q) { const float x0 = bf_lo(rw[i][j][q]), x1 = bf_hi(rw[i][j][q]); ss += x0 * x0; ss += x1 * x1; }
;                 rs[4 * i4 + i] = rsqrtf(wave_sum(ss) * (1.f / D) + EPS); } }
	v_lshlrev_b32_e32 v54, 16, v38
	v_and_b32_e32 v62, 0xffff0000, v38
	v_pk_fma_f32 v[44:45], v[54:55], v[54:55], v[44:45]
	v_and_b32_e32 v55, 0xffff0000, v35
	v_pk_fma_f32 v[44:45], v[62:63], v[62:63], v[44:45]
	v_lshlrev_b32_e32 v35, 16, v35
	v_lshlrev_b32_e32 v34, 16, v39
	v_and_b32_e32 v54, 0xffff0000, v39
	v_pk_fma_f32 v[34:35], v[34:35], v[34:35], v[44:45]
	v_lshlrev_b32_e32 v56, 16, v40
	v_pk_fma_f32 v[34:35], v[54:55], v[54:55], v[34:35]
	s_waitcnt lgkmcnt(0)
	v_pk_add_f32 v[50:51], v[50:51], v[52:53]
	s_waitcnt vmcnt(16)
	v_and_b32_e32 v38, 0xffff0000, v48
	v_lshlrev_b32_e32 v39, 16, v48
	v_pk_mul_f32 v[62:63], v[38:39], v[38:39]
	v_and_b32_e32 v39, 0xffff0000, v36
	v_and_b32_e32 v38, 0xffff0000, v40
	v_pk_fma_f32 v[34:35], v[56:57], v[56:57], v[34:35]
	v_and_b32_e32 v36, 0xffff0000, v41
	v_pk_fma_f32 v[34:35], v[38:39], v[38:39], v[34:35]
	v_lshlrev_b32_e32 v39, 16, v37
	v_lshlrev_b32_e32 v38, 16, v41
	v_and_b32_e32 v37, 0xffff0000, v37
	v_pk_fma_f32 v[34:35], v[38:39], v[38:39], v[34:35]
	v_and_b32_e32 v39, 0xffff0000, v42
	v_pk_fma_f32 v[34:35], v[36:37], v[36:37], v[34:35]
	v_lshlrev_b32_e32 v37, 16, v42
	v_lshlrev_b32_e32 v36, 16, v46
	v_and_b32_e32 v38, 0xffff0000, v46
	v_pk_fma_f32 v[34:35], v[36:37], v[36:37], v[34:35]
	v_lshlrev_b32_e32 v57, 16, v43
	v_pk_fma_f32 v[54:55], v[38:39], v[38:39], v[34:35]
	v_lshlrev_b32_e32 v56, 16, v47
	v_and_b32_e32 v64, 0xffff0000, v47
	v_pk_fma_f32 v[46:47], v[56:57], v[56:57], v[54:55]
	v_mov_b32_e32 v54, v63
	v_pk_fma_f32 v[46:47], v[64:65], v[64:65], v[46:47]
	v_mov_b32_e32 v55, v59
	v_and_b32_e32 v48, 0xffff0000, v49
	v_lshlrev_b32_e32 v49, 16, v49
	v_pk_add_f32 v[46:47], v[54:55], v[46:47]
	v_pk_mul_f32 v[48:49], v[48:49], v[48:49]
	v_mov_b32_e32 v63, v58
	s_waitcnt vmcnt(15)
	v_mov_b64_e32 v[34:35], v[142:143]
	v_mov_b64_e32 v[36:37], v[144:145]
	s_waitcnt vmcnt(14)
	v_mov_b64_e32 v[38:39], v[146:147]
	v_mov_b64_e32 v[40:41], v[148:149]
	s_waitcnt vmcnt(13)
	v_mov_b64_e32 v[80:81], v[150:151]
	v_mov_b64_e32 v[82:83], v[152:153]
	s_waitcnt vmcnt(12)
	v_mov_b64_e32 v[84:85], v[154:155]
	v_mov_b64_e32 v[86:87], v[156:157]
	s_waitcnt vmcnt(11)
	v_mov_b64_e32 v[42:43], v[158:159]
	v_mov_b64_e32 v[44:45], v[160:161]
	v_pk_add_f32 v[46:47], v[62:63], v[46:47]
	v_mov_b32_e32 v54, v49
	v_mov_b32_e32 v55, v61
	v_pk_add_f32 v[46:47], v[54:55], v[46:47]
	v_mov_b32_e32 v49, v60
	v_pk_add_f32 v[46:47], v[48:49], v[46:47]
	ds_bpermute_b32 v49, v1, v47
	ds_bpermute_b32 v48, v1, v46
	s_waitcnt vmcnt(10)
	v_mov_b64_e32 v[88:89], v[162:163]
	v_mov_b64_e32 v[90:91], v[164:165]
	s_waitcnt vmcnt(9)
	v_mov_b64_e32 v[92:93], v[166:167]
	v_mov_b64_e32 v[94:95], v[168:169]
	ds_bpermute_b32 v53, v223, v51
	ds_bpermute_b32 v52, v223, v50
	s_waitcnt lgkmcnt(2)
	v_pk_add_f32 v[54:55], v[46:47], v[48:49]
	s_waitcnt vmcnt(8)
	v_mov_b64_e32 v[46:47], v[170:171]
	v_mov_b64_e32 v[48:49], v[172:173]
	ds_bpermute_b32 v57, v201, v55
	ds_bpermute_b32 v56, v201, v54
	s_waitcnt lgkmcnt(2)
	v_pk_add_f32 v[50:51], v[50:51], v[52:53]
	s_waitcnt lgkmcnt(0)
	v_pk_add_f32 v[52:53], v[54:55], v[56:57]
	ds_bpermute_b32 v55, v220, v53
	ds_bpermute_b32 v54, v220, v52
	v_pk_fma_f32 v[50:51], v[50:51], s[38:39], v[78:79] op_sel_hi:[1,0,0]
	s_waitcnt lgkmcnt(0)
	v_pk_add_f32 v[52:53], v[52:53], v[54:55]
	ds_bpermute_b32 v55, v221, v53
	ds_bpermute_b32 v54, v221, v52
	v_mul_f32_e32 v56, 0x4b800000, v51
	v_cmp_gt_f32_e32 vcc, s88, v51
	v_cmp_gt_f32_e64 s[22:23], s88, v50
	s_waitcnt lgkmcnt(0)
	v_pk_add_f32 v[52:53], v[52:53], v[54:55]
	v_cndmask_b32_e32 v51, v51, v56, vcc
	v_rsq_f32_e32 v51, v51
	ds_bpermute_b32 v55, v222, v53
	ds_bpermute_b32 v54, v222, v52
	v_mul_f32_e32 v56, 0x45800000, v51
	v_cndmask_b32_e32 v246, v51, v56, vcc
	v_mul_f32_e32 v51, 0x4b800000, v50
	v_cndmask_b32_e64 v112, v50, v51, s[22:23]
	s_waitcnt lgkmcnt(0)
	v_pk_add_f32 v[96:97], v[52:53], v[54:55]
	s_waitcnt vmcnt(7)
	v_mov_b64_e32 v[50:51], v[174:175]
	v_mov_b64_e32 v[52:53], v[176:177]
	s_waitcnt vmcnt(6)
	v_mov_b64_e32 v[54:55], v[178:179]
	v_mov_b64_e32 v[56:57], v[180:181]
	s_waitcnt vmcnt(5)
	v_mov_b64_e32 v[70:71], v[182:183]
	v_mov_b64_e32 v[72:73], v[184:185]
	s_waitcnt vmcnt(4)
	v_mov_b64_e32 v[66:67], v[186:187]
	v_mov_b64_e32 v[68:69], v[188:189]
	s_waitcnt vmcnt(3)
	v_mov_b64_e32 v[58:59], v[190:191]
	v_mov_b64_e32 v[60:61], v[192:193]
	s_waitcnt vmcnt(2)
	v_mov_b64_e32 v[62:63], v[114:115]
	v_mov_b64_e32 v[64:65], v[116:117]
	s_waitcnt vmcnt(1)
	v_mov_b64_e32 v[74:75], v[118:119]
	v_mov_b64_e32 v[76:77], v[120:121]
	ds_bpermute_b32 v99, v223, v97
	ds_bpermute_b32 v98, v223, v96
	s_waitcnt vmcnt(1)
	v_lshlrev_b32_e32 v107, 16, v34
	v_and_b32_e32 v109, 0xffff0000, v34
	v_and_b32_e32 v111, 0xffff0000, v35
	s_waitcnt vmcnt(1)
	v_and_b32_e32 v101, 0xffff0000, v38
	s_waitcnt vmcnt(1)
	v_lshlrev_b32_e32 v106, 16, v42
	v_and_b32_e32 v108, 0xffff0000, v42
	v_pk_mul_f32 v[106:107], v[106:107], v[106:107]
	v_and_b32_e32 v110, 0xffff0000, v43
	v_pk_fma_f32 v[106:107], v[108:109], v[108:109], v[106:107]
	v_lshlrev_b32_e32 v109, 16, v35
	v_lshlrev_b32_e32 v108, 16, v43
	v_pk_fma_f32 v[106:107], v[108:109], v[108:109], v[106:107]
	v_lshlrev_b32_e32 v109, 16, v36
	v_pk_fma_f32 v[106:107], v[110:111], v[110:111], v[106:107]
	v_lshlrev_b32_e32 v108, 16, v44
	v_and_b32_e32 v111, 0xffff0000, v36
	v_and_b32_e32 v110, 0xffff0000, v44
	v_pk_fma_f32 v[106:107], v[108:109], v[108:109], v[106:107]
	v_lshlrev_b32_e32 v109, 16, v37
	v_pk_fma_f32 v[106:107], v[110:111], v[110:111], v[106:107]
	v_lshlrev_b32_e32 v108, 16, v45
	v_pk_fma_f32 v[106:107], v[108:109], v[108:109], v[106:107]
	v_and_b32_e32 v109, 0xffff0000, v37
	v_and_b32_e32 v108, 0xffff0000, v45
	v_lshlrev_b32_e32 v111, 16, v38
	s_waitcnt vmcnt(1)
; __device__ __forceinline__ float bf_lo(unsigned w) { return __uint_as_float(w << 16); }
; __device__ __forceinline__ float bf_hi(unsigned w) { return __uint_as_float(w & 0xffff0000u); }
; __device__ __forceinline__ void phase_nrr(const Frame& F, const Args& a, int l, const bf16_t* XA, const float* g, const float* modl, unsigned char* XN8) {
;     ...
;         const int tb = tile * 64 + w * 8, b = tb / S;
;         __syncthreads();
;         if (F.tid < NE) hist[F.tid] = 0;
;         float rs[8];
; #pragma unroll
;         for (int i4 = 0; i4 < 2; ++i4) { u32x4 rw[4][4];
; #pragma unroll
;             for (int i = 0; i < 4; ++i)
; #pragma unroll
;                 for (int j = 0; j < 4; ++j) rw[i][j] = *(const u32x4*)(XA + (size_t)(tb + 4 * i4 + i) * D + (j * 64 + lane) * 8);
; #pragma unroll
;             for (int i = 0; i < 4; ++i) { float ss = 0.f;
; #pragma unroll
;                 for (int j = 0; j < 4; ++j)
; #pragma unroll
;                     for (int q = 0; q < 4; ++q) { const float x0 = bf_lo(rw[i][j][q]), x1 = bf_hi(rw[i][j][q]); ss += x0 * x0; ss += x1 * x1; }
;                 rs[4 * i4 + i] = rsqrtf(wave_sum(ss) * (1.f / D) + EPS); } }
	v_lshlrev_b32_e32 v110, 16, v46
	v_pk_fma_f32 v[106:107], v[108:109], v[108:109], v[106:107]
	v_and_b32_e32 v100, 0xffff0000, v46
	v_pk_fma_f32 v[106:107], v[110:111], v[110:111], v[106:107]
	v_and_b32_e32 v109, 0xffff0000, v39
	v_pk_fma_f32 v[100:101], v[100:101], v[100:101], v[106:107]
	v_lshlrev_b32_e32 v107, 16, v39
	v_lshlrev_b32_e32 v106, 16, v47
	v_and_b32_e32 v108, 0xffff0000, v47
	v_pk_fma_f32 v[100:101], v[106:107], v[106:107], v[100:101]
	v_lshlrev_b32_e32 v107, 16, v40
	v_pk_fma_f32 v[100:101], v[108:109], v[108:109], v[100:101]
	v_lshlrev_b32_e32 v106, 16, v48
	v_and_b32_e32 v109, 0xffff0000, v40
	v_and_b32_e32 v108, 0xffff0000, v48
	v_pk_fma_f32 v[100:101], v[106:107], v[106:107], v[100:101]
	v_lshlrev_b32_e32 v107, 16, v41
	v_pk_fma_f32 v[100:101], v[108:109], v[108:109], v[100:101]
	v_lshlrev_b32_e32 v106, 16, v49
	v_and_b32_e32 v109, 0xffff0000, v41
	v_and_b32_e32 v108, 0xffff0000, v49
	v_pk_fma_f32 v[100:101], v[106:107], v[106:107], v[100:101]
	v_lshlrev_b32_e32 v107, 16, v80
	v_pk_fma_f32 v[100:101], v[108:109], v[108:109], v[100:101]
	v_lshlrev_b32_e32 v106, 16, v88
	v_and_b32_e32 v109, 0xffff0000, v80
	v_and_b32_e32 v108, 0xffff0000, v88
	v_pk_fma_f32 v[100:101], v[106:107], v[106:107], v[100:101]
	v_and_b32_e32 v107, 0xffff0000, v81
	v_pk_fma_f32 v[100:101], v[108:109], v[108:109], v[100:101]
	v_lshlrev_b32_e32 v81, 16, v81
	v_lshlrev_b32_e32 v80, 16, v89
	v_and_b32_e32 v106, 0xffff0000, v89
	v_pk_fma_f32 v[80:81], v[80:81], v[80:81], v[100:101]
	v_lshlrev_b32_e32 v103, 16, v82
	v_lshlrev_b32_e32 v102, 16, v90
	v_pk_fma_f32 v[80:81], v[106:107], v[106:107], v[80:81]
	v_and_b32_e32 v101, 0xffff0000, v82
	v_and_b32_e32 v100, 0xffff0000, v90
	v_pk_fma_f32 v[80:81], v[102:103], v[102:103], v[80:81]
	v_and_b32_e32 v82, 0xffff0000, v91
	v_pk_fma_f32 v[80:81], v[100:101], v[100:101], v[80:81]
	v_lshlrev_b32_e32 v101, 16, v83
	v_lshlrev_b32_e32 v100, 16, v91
	v_and_b32_e32 v83, 0xffff0000, v83
	v_pk_fma_f32 v[80:81], v[100:101], v[100:101], v[80:81]
	v_and_b32_e32 v91, 0xffff0000, v84
	v_pk_fma_f32 v[80:81], v[82:83], v[82:83], v[80:81]
	v_lshlrev_b32_e32 v83, 16, v84
	v_lshlrev_b32_e32 v82, 16, v92
	v_and_b32_e32 v90, 0xffff0000, v92
	v_pk_fma_f32 v[80:81], v[82:83], v[82:83], v[80:81]
	v_and_b32_e32 v104, 0xffff0000, v86
	v_lshlrev_b32_e32 v105, 16, v86
	v_and_b32_e32 v88, 0xffff0000, v94
	v_lshlrev_b32_e32 v89, 16, v94
	v_pk_fma_f32 v[80:81], v[90:91], v[90:91], v[80:81]
	v_lshlrev_b32_e32 v83, 16, v85
	v_lshlrev_b32_e32 v82, 16, v93
	v_pk_mul_f32 v[104:105], v[104:105], v[104:105]
	v_pk_mul_f32 v[88:89], v[88:89], v[88:89]
	v_and_b32_e32 v85, 0xffff0000, v85
	v_and_b32_e32 v84, 0xffff0000, v93
	v_pk_fma_f32 v[80:81], v[82:83], v[82:83], v[80:81]
	v_mov_b32_e32 v82, v89
	v_pk_fma_f32 v[80:81], v[84:85], v[84:85], v[80:81]
	v_mov_b32_e32 v83, v105
	v_and_b32_e32 v86, 0xffff0000, v87
	v_lshlrev_b32_e32 v87, 16, v87
	v_pk_add_f32 v[80:81], v[82:83], v[80:81]
	v_and_b32_e32 v82, 0xffff0000, v95
	v_lshlrev_b32_e32 v83, 16, v95
	v_pk_mul_f32 v[86:87], v[86:87], v[86:87]
	v_pk_mul_f32 v[82:83], v[82:83], v[82:83]
	v_mov_b32_e32 v89, v104
	v_pk_add_f32 v[80:81], v[88:89], v[80:81]
	v_mov_b32_e32 v84, v83
	v_mov_b32_e32 v85, v87
	v_pk_add_f32 v[80:81], v[84:85], v[80:81]
	v_mov_b32_e32 v83, v86
	v_pk_add_f32 v[80:81], v[82:83], v[80:81]
	ds_bpermute_b32 v83, v1, v81
	ds_bpermute_b32 v82, v1, v80
	s_waitcnt lgkmcnt(2)
	v_pk_add_f32 v[84:85], v[96:97], v[98:99]
	s_waitcnt vmcnt(1)
	v_lshlrev_b32_e32 v97, 16, v50
	s_waitcnt vmcnt(1)
	v_lshlrev_b32_e32 v96, 16, v58
	v_and_b32_e32 v99, 0xffff0000, v50
	s_waitcnt lgkmcnt(0)
	v_pk_add_f32 v[86:87], v[80:81], v[82:83]
	s_waitcnt vmcnt(0)
	v_mov_b64_e32 v[80:81], v[126:127]
	v_mov_b64_e32 v[82:83], v[128:129]
	v_and_b32_e32 v98, 0xffff0000, v58
	v_pk_mul_f32 v[96:97], v[96:97], v[96:97]
	v_and_b32_e32 v101, 0xffff0000, v51
	v_pk_fma_f32 v[96:97], v[98:99], v[98:99], v[96:97]
	v_lshlrev_b32_e32 v99, 16, v51
	v_lshlrev_b32_e32 v98, 16, v59
	v_and_b32_e32 v100, 0xffff0000, v59
	v_pk_fma_f32 v[96:97], v[98:99], v[98:99], v[96:97]
	v_rsq_f32_e32 v90, v112
	v_pk_fma_f32 v[96:97], v[100:101], v[100:101], v[96:97]
	v_lshlrev_b32_e32 v99, 16, v52
	v_lshlrev_b32_e32 v98, 16, v60
	v_and_b32_e32 v101, 0xffff0000, v52
	v_and_b32_e32 v100, 0xffff0000, v60
	v_pk_fma_f32 v[96:97], v[98:99], v[98:99], v[96:97]
	v_pk_fma_f32 v[84:85], v[84:85], s[38:39], v[78:79] op_sel_hi:[1,0,0]
	v_pk_fma_f32 v[96:97], v[100:101], v[100:101], v[96:97]
	v_lshlrev_b32_e32 v99, 16, v53
	v_lshlrev_b32_e32 v98, 16, v61
	v_mul_f32_e32 v91, 0x4b800000, v85
	v_cmp_gt_f32_e32 vcc, s88, v85
	v_pk_fma_f32 v[96:97], v[98:99], v[98:99], v[96:97]
	v_and_b32_e32 v99, 0xffff0000, v53
	v_and_b32_e32 v98, 0xffff0000, v61
	v_cndmask_b32_e32 v85, v85, v91, vcc
	v_mul_f32_e32 v91, 0x45800000, v90
	v_lshlrev_b32_e32 v101, 16, v54
	s_waitcnt vmcnt(2)
	v_lshlrev_b32_e32 v100, 16, v62
	v_pk_fma_f32 v[96:97], v[98:99], v[98:99], v[96:97]
	v_cndmask_b32_e64 v247, v90, v91, s[22:23]
	v_and_b32_e32 v91, 0xffff0000, v54
	v_and_b32_e32 v90, 0xffff0000, v62
	v_pk_fma_f32 v[96:97], v[100:101], v[100:101], v[96:97]
	v_and_b32_e32 v99, 0xffff0000, v55
	v_pk_fma_f32 v[90:91], v[90:91], v[90:91], v[96:97]
	v_lshlrev_b32_e32 v97, 16, v55
	v_lshlrev_b32_e32 v96, 16, v63
	v_and_b32_e32 v98, 0xffff0000, v63
	v_pk_fma_f32 v[90:91], v[96:97], v[96:97], v[90:91]
	v_lshlrev_b32_e32 v97, 16, v56
	v_pk_fma_f32 v[90:91], v[98:99], v[98:99], v[90:91]
	v_lshlrev_b32_e32 v96, 16, v64
	v_and_b32_e32 v99, 0xffff0000, v56
	v_and_b32_e32 v98, 0xffff0000, v64
	v_pk_fma_f32 v[90:91], v[96:97], v[96:97], v[90:91]
	v_lshlrev_b32_e32 v97, 16, v57
	v_pk_fma_f32 v[90:91], v[98:99], v[98:99], v[90:91]
	v_lshlrev_b32_e32 v96, 16, v65
	v_and_b32_e32 v99, 0xffff0000, v57
	v_and_b32_e32 v98, 0xffff0000, v65
	v_pk_fma_f32 v[90:91], v[96:97], v[96:97], v[90:91]
	v_lshlrev_b32_e32 v97, 16, v70
	v_pk_fma_f32 v[90:91], v[98:99], v[98:99], v[90:91]
	s_waitcnt vmcnt(1)
; __device__ __forceinline__ float bf_lo(unsigned w) { return __uint_as_float(w << 16); }
; __device__ __forceinline__ float bf_hi(unsigned w) { return __uint_as_float(w & 0xffff0000u); }
; __device__ __forceinline__ void phase_nrr(const Frame& F, const Args& a, int l, const bf16_t* XA, const float* g, const float* modl, unsigned char* XN8) {
;     ...
;             for (int i = 0; i < 4; ++i) { float ss = 0.f;
; #pragma unroll
;                 for (int j = 0; j < 4; ++j)
; #pragma unroll
;                     for (int q = 0; q < 4; ++q) { const float x0 = bf_lo(rw[i][j][q]), x1 = bf_hi(rw[i][j][q]); ss += x0 * x0; ss += x1 * x1; }
;                 rs[4 * i4 + i] = rsqrtf(wave_sum(ss) * (1.f / D) + EPS); } }
;         f32x4 acc[4] = {{0.f, 0.f, 0.f, 0.f}, {0.f, 0.f, 0.f, 0.f}, {0.f, 0.f, 0.f, 0.f}, {0.f, 0.f, 0.f, 0.f}};
;         u32x4 raw[8][2];
; #pragma unroll
;         for (int i = 0; i < 8; ++i)
; #pragma unroll
;             for (int jj = 0; jj < 2; ++jj) raw[i][jj] = __builtin_nontemporal_load((const u32x4*)(XA + (size_t)(tb + i) * D + (jj * 64 + lane) * 8));
; #pragma unroll 1
;         for (int h = 0; h < 2; ++h) {
;             const bf16_t* wrow = Wr + (size_t)(16 * eb + fr) * D + h * 1024 + 512 * kq + 8 * fq;
;             bf16x8 bv[16];
; #pragma unroll
;             for (int kb = 0; kb < 16; ++kb) bv[kb] = *(const bf16x8*)(wrow + 32 * kb);
;             float gs[2][8], shv[2][8];
; #pragma unroll
;             for (int jj = 0; jj < 2; ++jj) { const int d = ((2 * h + jj) * 64 + lane) * 8; const float* sh = modl + (size_t)b * MODW + 3 * D; const float* sc = modl + (size_t)b * MODW + 4 * D;
	v_lshlrev_b32_e32 v96, 16, v74
	v_and_b32_e32 v99, 0xffff0000, v70
	v_and_b32_e32 v98, 0xffff0000, v74
	v_pk_fma_f32 v[90:91], v[96:97], v[96:97], v[90:91]
	v_and_b32_e32 v97, 0xffff0000, v71
	v_pk_fma_f32 v[90:91], v[98:99], v[98:99], v[90:91]
	v_lshlrev_b32_e32 v71, 16, v71
	v_lshlrev_b32_e32 v70, 16, v75
	v_and_b32_e32 v96, 0xffff0000, v75
	v_pk_fma_f32 v[70:71], v[70:71], v[70:71], v[90:91]
	v_lshlrev_b32_e32 v93, 16, v72
	v_lshlrev_b32_e32 v92, 16, v76
	v_pk_fma_f32 v[70:71], v[96:97], v[96:97], v[70:71]
	v_and_b32_e32 v91, 0xffff0000, v72
	v_and_b32_e32 v90, 0xffff0000, v76
	v_pk_fma_f32 v[70:71], v[92:93], v[92:93], v[70:71]
	v_and_b32_e32 v72, 0xffff0000, v77
	v_pk_fma_f32 v[70:71], v[90:91], v[90:91], v[70:71]
	v_lshlrev_b32_e32 v91, 16, v73
	v_lshlrev_b32_e32 v90, 16, v77
	v_and_b32_e32 v73, 0xffff0000, v73
	v_pk_fma_f32 v[70:71], v[90:91], v[90:91], v[70:71]
	v_and_b32_e32 v77, 0xffff0000, v66
	v_pk_fma_f32 v[70:71], v[72:73], v[72:73], v[70:71]
	v_lshlrev_b32_e32 v73, 16, v66
	v_and_b32_e32 v94, 0xffff0000, v68
	s_waitcnt vmcnt(0)
	v_lshlrev_b32_e32 v72, 16, v80
	v_and_b32_e32 v76, 0xffff0000, v80
	v_pk_fma_f32 v[70:71], v[72:73], v[72:73], v[70:71]
	v_lshlrev_b32_e32 v95, 16, v68
	v_and_b32_e32 v74, 0xffff0000, v82
	v_lshlrev_b32_e32 v75, 16, v82
	v_pk_fma_f32 v[70:71], v[76:77], v[76:77], v[70:71]
	v_lshlrev_b32_e32 v73, 16, v67
	v_lshlrev_b32_e32 v72, 16, v81
	v_pk_mul_f32 v[94:95], v[94:95], v[94:95]
	v_pk_mul_f32 v[74:75], v[74:75], v[74:75]
	v_and_b32_e32 v67, 0xffff0000, v67
	v_and_b32_e32 v66, 0xffff0000, v81
	v_pk_fma_f32 v[70:71], v[72:73], v[72:73], v[70:71]
	v_and_b32_e32 v68, 0xffff0000, v69
	v_pk_fma_f32 v[66:67], v[66:67], v[66:67], v[70:71]
	v_mov_b32_e32 v70, v75
	v_mov_b32_e32 v71, v95
	v_lshlrev_b32_e32 v69, 16, v69
	v_pk_add_f32 v[66:67], v[70:71], v[66:67]
	v_and_b32_e32 v70, 0xffff0000, v83
	v_lshlrev_b32_e32 v71, 16, v83
	v_pk_mul_f32 v[68:69], v[68:69], v[68:69]
	v_pk_mul_f32 v[70:71], v[70:71], v[70:71]
	v_mov_b32_e32 v75, v94
	v_pk_add_f32 v[66:67], v[74:75], v[66:67]
	v_mov_b32_e32 v72, v71
	v_mov_b32_e32 v73, v69
	v_pk_add_f32 v[66:67], v[72:73], v[66:67]
	v_mov_b32_e32 v71, v68
	ds_bpermute_b32 v89, v201, v87
	ds_bpermute_b32 v88, v201, v86
	v_pk_add_f32 v[66:67], v[70:71], v[66:67]
	ds_bpermute_b32 v69, v1, v67
	ds_bpermute_b32 v68, v1, v66
	v_rsq_f32_e32 v85, v85
	s_waitcnt lgkmcnt(2)
	v_pk_add_f32 v[86:87], v[86:87], v[88:89]
	ds_bpermute_b32 v89, v220, v87
	ds_bpermute_b32 v88, v220, v86
	s_waitcnt lgkmcnt(2)
	v_pk_add_f32 v[66:67], v[66:67], v[68:69]
	ds_bpermute_b32 v69, v201, v67
	ds_bpermute_b32 v68, v201, v66
	v_mul_f32_e32 v102, 0x45800000, v85
	s_waitcnt lgkmcnt(2)
	v_pk_add_f32 v[86:87], v[86:87], v[88:89]
	ds_bpermute_b32 v89, v221, v87
	ds_bpermute_b32 v88, v221, v86
	s_waitcnt lgkmcnt(2)
	v_pk_add_f32 v[66:67], v[66:67], v[68:69]
	ds_bpermute_b32 v69, v220, v67
	ds_bpermute_b32 v68, v220, v66
	v_cndmask_b32_e32 v248, v85, v102, vcc
	s_waitcnt lgkmcnt(2)
	v_pk_add_f32 v[70:71], v[86:87], v[88:89]
	ds_bpermute_b32 v73, v222, v71
	ds_bpermute_b32 v72, v222, v70
	s_waitcnt lgkmcnt(2)
	v_pk_add_f32 v[66:67], v[66:67], v[68:69]
	ds_bpermute_b32 v69, v221, v67
	ds_bpermute_b32 v68, v221, v66
	v_mul_f32_e32 v103, 0x4b800000, v84
	s_waitcnt lgkmcnt(2)
	v_pk_add_f32 v[70:71], v[70:71], v[72:73]
	ds_bpermute_b32 v73, v223, v71
	ds_bpermute_b32 v72, v223, v70
	s_waitcnt lgkmcnt(2)
	v_pk_add_f32 v[66:67], v[66:67], v[68:69]
	ds_bpermute_b32 v69, v222, v67
	ds_bpermute_b32 v68, v222, v66
	v_cmp_gt_f32_e64 s[22:23], s88, v84
	s_waitcnt lgkmcnt(2)
	v_pk_add_f32 v[70:71], v[70:71], v[72:73]
	v_mov_b32_e32 v110, 0
	v_pk_fma_f32 v[70:71], v[70:71], s[38:39], v[78:79] op_sel_hi:[1,0,0]
	s_waitcnt lgkmcnt(0)
	v_pk_add_f32 v[66:67], v[66:67], v[68:69]
	v_mul_f32_e32 v72, 0x4b800000, v71
	v_cmp_gt_f32_e32 vcc, s88, v71
	ds_bpermute_b32 v69, v223, v67
	ds_bpermute_b32 v68, v223, v66
	v_cndmask_b32_e32 v71, v71, v72, vcc
	v_cndmask_b32_e64 v74, v84, v103, s[22:23]
	v_rsq_f32_e32 v71, v71
	v_rsq_f32_e32 v74, v74
	v_mul_f32_e32 v72, 0x4b800000, v70
	v_cmp_gt_f32_e64 s[24:25], s88, v70
	s_waitcnt lgkmcnt(0)
	v_pk_add_f32 v[66:67], v[66:67], v[68:69]
	v_mul_f32_e32 v75, 0x45800000, v74
	v_cndmask_b32_e64 v70, v70, v72, s[24:25]
	v_mul_f32_e32 v72, 0x45800000, v71
	v_pk_fma_f32 v[66:67], v[66:67], s[38:39], v[78:79] op_sel_hi:[1,0,0]
	v_cndmask_b32_e32 v250, v71, v72, vcc
	v_mul_f32_e32 v68, 0x4b800000, v67
	v_cmp_gt_f32_e32 vcc, s88, v67
	v_cndmask_b32_e64 v249, v74, v75, s[22:23]
	v_cmp_gt_f32_e64 s[22:23], s88, v66
	v_cndmask_b32_e32 v67, v67, v68, vcc
	v_mul_f32_e32 v68, 0x4b800000, v66
	v_rsq_f32_e32 v67, v67
	v_cndmask_b32_e64 v66, v66, v68, s[22:23]
	v_rsq_f32_e32 v66, v66
	v_rsq_f32_e32 v70, v70
	v_mul_f32_e32 v68, 0x45800000, v67
	v_cndmask_b32_e32 v252, v67, v68, vcc
	v_mul_f32_e32 v67, 0x45800000, v66
	v_mul_f32_e32 v71, 0x45800000, v70
	v_cndmask_b32_e64 v253, v66, v67, s[22:23]
	s_mul_hi_i32 s22, s36, 0xc000
	s_mul_i32 s36, s36, 0xc000
	v_cndmask_b32_e64 v251, v70, v71, s[24:25]
	s_add_u32 s24, s69, s36
	s_addc_u32 s25, s70, s22
	s_add_u32 s22, s24, 0x6000
	s_addc_u32 s23, s25, 0
	s_add_u32 s24, s24, 0x8000
	s_addc_u32 s25, s25, 0
	s_lshl_b64 s[46:47], s[44:45], 11
	s_add_u32 s46, s39, s46
	s_addc_u32 s47, s71, s47
	s_lshl_b64 s[48:49], s[42:43], 11
	s_add_u32 s48, s39, s48
	s_addc_u32 s49, s71, s49
	s_lshl_b64 s[50:51], s[40:41], 11
	s_add_u32 s50, s39, s50
	s_addc_u32 s51, s71, s51
	s_lshl_b64 s[52:53], s[4:5], 11
	s_add_u32 s52, s39, s52
	s_addc_u32 s53, s71, s53
	s_lshl_b64 s[54:55], s[2:3], 11
	s_add_u32 s54, s39, s54
	s_addc_u32 s55, s71, s55
	s_lshl_b64 s[56:57], s[56:57], 11
	s_add_u32 s56, s39, s56
	s_addc_u32 s57, s71, s57
	s_lshl_b64 s[58:59], s[58:59], 11
	s_add_u32 s58, s39, s58
	s_addc_u32 s59, s71, s59
	s_lshl_b64 s[60:61], s[60:61], 11
	s_add_u32 s60, s39, s60
	s_addc_u32 s61, s71, s61
	s_mov_b32 s36, 0
	v_mov_b32_e32 v111, v110
	v_mov_b32_e32 v112, v110
	v_mov_b32_e32 v113, v110
	v_mov_b32_e32 v118, v110
	v_mov_b32_e32 v119, v110
	v_mov_b32_e32 v120, v110
	v_mov_b32_e32 v121, v110
	v_mov_b32_e32 v126, v110
	v_mov_b32_e32 v127, v110
	v_mov_b32_e32 v128, v110
	v_mov_b32_e32 v129, v110
	v_mov_b32_e32 v130, v110
	v_mov_b32_e32 v131, v110
	v_mov_b32_e32 v132, v110
	v_mov_b32_e32 v133, v110
	s_branch .LBB0_531

; __device__ __forceinline__ float bf_lo(unsigned w) { return __uint_as_float(w << 16); }
; __device__ __forceinline__ float bf_hi(unsigned w) { return __uint_as_float(w & 0xffff0000u); }
; __device__ __forceinline__ void phase_nrr(const Frame& F, const Args& a, int l, const bf16_t* XA, const float* g, const float* modl, unsigned char* XN8) {
;     ...
;     for (int tile = F.bid; tile < T / 64; tile += F.G) {
;         const int tb = tile * 64 + w * 8, b = tb / S;
;         __syncthreads();
;         if (F.tid < NE) hist[F.tid] = 0;
;         float rs[8];
; #pragma unroll
;         for (int i4 = 0; i4 < 2; ++i4) { u32x4 rw[4][4];
; #pragma unroll
;             for (int i = 0; i < 4; ++i)
; #pragma unroll
;                 for (int j = 0; j < 4; ++j) rw[i][j] = *(const u32x4*)(XA + (size_t)(tb + 4 * i4 + i) * D + (j * 64 + lane) * 8);
; #pragma unroll
;             for (int i = 0; i < 4; ++i) { float ss = 0.f;
; #pragma unroll
;                 for (int j = 0; j < 4; ++j)
; #pragma unroll
;                     for (int q = 0; q < 4; ++q) { const float x0 = bf_lo(rw[i][j][q]), x1 = bf_hi(rw[i][j][q]); ss += x0 * x0; ss += x1 * x1; }
;                 rs[4 * i4 + i] = rsqrtf(wave_sum(ss) * (1.f / D) + EPS); } }
.LBB0_1300:
	s_waitcnt vmcnt(0)
	s_barrier
	s_and_saveexec_b64 s[2:3], s[18:19]
	ds_write_b32 v241, v195
	s_or_b64 exec, exec, s[2:3]
	s_lshl_b32 s86, s85, 6
	s_add_i32 s24, s86, s71
	s_ashr_i32 s25, s24, 31
	s_lshl_b64 s[2:3], s[24:25], 12
	v_lshl_add_u64 v[204:205], v[202:203], 0, s[2:3]
	s_or_b32 s56, s24, 1
	global_load_dwordx4 v[2:5], v[204:205], off offset:1024
	global_load_dwordx4 v[38:41], v[204:205], off offset:2048
	global_load_dwordx4 v[46:49], v[204:205], off offset:3072
	global_load_dwordx4 v[6:9], v[204:205], off
	s_ashr_i32 s57, s56, 31
	s_lshl_b64 s[2:3], s[56:57], 12
	v_lshl_add_u64 v[206:207], v[202:203], 0, s[2:3]
	global_load_dwordx4 v[10:13], v[206:207], off
	global_load_dwordx4 v[14:17], v[206:207], off offset:1024
	global_load_dwordx4 v[50:53], v[206:207], off offset:2048
	global_load_dwordx4 v[54:57], v[206:207], off offset:3072
	s_or_b32 s54, s24, 2
	s_or_b32 s4, s24, 3
	s_ashr_i32 s55, s54, 31
	s_ashr_i32 s5, s4, 31
	s_lshl_b64 s[2:3], s[54:55], 12
	s_lshl_b64 s[20:21], s[4:5], 12
	v_lshl_add_u64 v[208:209], v[202:203], 0, s[2:3]
	v_lshl_add_u64 v[210:211], v[202:203], 0, s[20:21]
	global_load_dwordx4 v[18:21], v[208:209], off
	global_load_dwordx4 v[22:25], v[208:209], off offset:1024
	global_load_dwordx4 v[34:37], v[208:209], off offset:2048
	global_load_dwordx4 v[42:45], v[208:209], off offset:3072
	global_load_dwordx4 v[26:29], v[210:211], off
	global_load_dwordx4 v[30:33], v[210:211], off offset:1024
	s_or_b32 s2, s24, 4
	s_ashr_i32 s3, s2, 31
	s_or_b32 s40, s24, 5
	s_lshl_b64 s[20:21], s[2:3], 12
	s_ashr_i32 s41, s40, 31
	v_lshl_add_u64 v[212:213], v[202:203], 0, s[20:21]
	s_lshl_b64 s[20:21], s[40:41], 12
	v_lshl_add_u64 v[214:215], v[202:203], 0, s[20:21]
	s_mov_b32 s20, 0x358637bd
	s_or_b32 s58, s24, 6
	s_ashr_i32 s59, s58, 31
	s_or_b32 s60, s24, 7
	s_lshl_b64 s[22:23], s[58:59], 12
	s_ashr_i32 s61, s60, 31
	v_lshl_add_u64 v[216:217], v[202:203], 0, s[22:23]
	s_lshl_b64 s[22:23], s[60:61], 12
	v_lshl_add_u64 v[218:219], v[202:203], 0, s[22:23]
	s_mov_b32 s50, 0
	s_mov_b64 s[62:63], -1
	s_mov_b64 s[66:67], 0
	global_load_dwordx4 v[134:137], v[210:211], off offset:2048
	global_load_dwordx4 v[138:141], v[210:211], off offset:3072
	global_load_dwordx4 v[142:145], v[212:213], off
	global_load_dwordx4 v[146:149], v[212:213], off offset:1024
	global_load_dwordx4 v[150:153], v[212:213], off offset:2048
	global_load_dwordx4 v[154:157], v[212:213], off offset:3072
	global_load_dwordx4 v[158:161], v[214:215], off
	global_load_dwordx4 v[162:165], v[214:215], off offset:2048
	global_load_dwordx4 v[166:169], v[214:215], off offset:3072
	global_load_dwordx4 v[170:173], v[214:215], off offset:1024
	global_load_dwordx4 v[174:177], v[216:217], off
	global_load_dwordx4 v[178:181], v[216:217], off offset:1024
	global_load_dwordx4 v[182:185], v[216:217], off offset:2048
	global_load_dwordx4 v[186:189], v[216:217], off offset:3072
	global_load_dwordx4 v[190:193], v[218:219], off
	global_load_dwordx4 v[114:117], v[218:219], off offset:1024
	global_load_dwordx4 v[118:121], v[218:219], off offset:2048
	global_load_dwordx4 v[126:129], v[218:219], off offset:3072
	s_waitcnt vmcnt(31)
	v_lshlrev_b32_e32 v81, 16, v2
	v_and_b32_e32 v59, 0xffff0000, v2
	v_lshlrev_b32_e32 v83, 16, v3
	s_waitcnt vmcnt(28)
	v_lshlrev_b32_e32 v65, 16, v6
	s_waitcnt vmcnt(27)
	v_lshlrev_b32_e32 v64, 16, v10
	v_and_b32_e32 v67, 0xffff0000, v6
	v_and_b32_e32 v66, 0xffff0000, v10
	v_pk_mul_f32 v[64:65], v[64:65], v[64:65]
	v_lshlrev_b32_e32 v69, 16, v7
	v_lshlrev_b32_e32 v68, 16, v11
	v_pk_fma_f32 v[64:65], v[66:67], v[66:67], v[64:65]
	v_and_b32_e32 v71, 0xffff0000, v7
	v_and_b32_e32 v70, 0xffff0000, v11
	v_pk_fma_f32 v[64:65], v[68:69], v[68:69], v[64:65]
	v_lshlrev_b32_e32 v73, 16, v8
	v_lshlrev_b32_e32 v72, 16, v12
	v_pk_fma_f32 v[64:65], v[70:71], v[70:71], v[64:65]
	v_and_b32_e32 v75, 0xffff0000, v8
	v_and_b32_e32 v74, 0xffff0000, v12
	v_pk_fma_f32 v[64:65], v[72:73], v[72:73], v[64:65]
	v_lshlrev_b32_e32 v77, 16, v9
	v_lshlrev_b32_e32 v76, 16, v13
	v_pk_fma_f32 v[64:65], v[74:75], v[74:75], v[64:65]
	v_and_b32_e32 v79, 0xffff0000, v9
	v_and_b32_e32 v78, 0xffff0000, v13
	v_pk_fma_f32 v[64:65], v[76:77], v[76:77], v[64:65]
	s_waitcnt vmcnt(26)
	v_lshlrev_b32_e32 v80, 16, v14
	v_pk_fma_f32 v[64:65], v[78:79], v[78:79], v[64:65]
	v_and_b32_e32 v58, 0xffff0000, v14
	v_pk_fma_f32 v[64:65], v[80:81], v[80:81], v[64:65]
	v_lshlrev_b32_e32 v82, 16, v15
	v_pk_fma_f32 v[58:59], v[58:59], v[58:59], v[64:65]
	v_and_b32_e32 v85, 0xffff0000, v3
	v_and_b32_e32 v84, 0xffff0000, v15
	v_pk_fma_f32 v[58:59], v[82:83], v[82:83], v[58:59]
	v_lshlrev_b32_e32 v87, 16, v4
	v_lshlrev_b32_e32 v86, 16, v16
	v_pk_fma_f32 v[58:59], v[84:85], v[84:85], v[58:59]
	v_and_b32_e32 v89, 0xffff0000, v4
	v_and_b32_e32 v88, 0xffff0000, v16
	v_pk_fma_f32 v[58:59], v[86:87], v[86:87], v[58:59]
	v_lshlrev_b32_e32 v91, 16, v5
	v_lshlrev_b32_e32 v90, 16, v17
	v_pk_fma_f32 v[58:59], v[88:89], v[88:89], v[58:59]
	v_and_b32_e32 v93, 0xffff0000, v5
	v_and_b32_e32 v92, 0xffff0000, v17
	v_pk_fma_f32 v[58:59], v[90:91], v[90:91], v[58:59]
	v_lshlrev_b32_e32 v95, 16, v38
	s_waitcnt vmcnt(25)
; __device__ __forceinline__ float bf_lo(unsigned w) { return __uint_as_float(w << 16); }
; __device__ __forceinline__ float bf_hi(unsigned w) { return __uint_as_float(w & 0xffff0000u); }
; __device__ __forceinline__ void phase_nrr(const Frame& F, const Args& a, int l, const bf16_t* XA, const float* g, const float* modl, unsigned char* XN8) {
;     ...
;         for (int i4 = 0; i4 < 2; ++i4) { u32x4 rw[4][4];
; #pragma unroll
;             for (int i = 0; i < 4; ++i)
; #pragma unroll
;                 for (int j = 0; j < 4; ++j) rw[i][j] = *(const u32x4*)(XA + (size_t)(tb + 4 * i4 + i) * D + (j * 64 + lane) * 8);
; #pragma unroll
;             for (int i = 0; i < 4; ++i) { float ss = 0.f;
; #pragma unroll
;                 for (int j = 0; j < 4; ++j)
; #pragma unroll
;                     for (int q = 0; q < 4; ++q) { const float x0 = bf_lo(rw[i][j][q]), x1 = bf_hi(rw[i][j][q]); ss += x0 * x0; ss += x1 * x1; }
;                 rs[4 * i4 + i] = rsqrtf(wave_sum(ss) * (1.f / D) + EPS); } }
	v_lshlrev_b32_e32 v94, 16, v50
	v_pk_fma_f32 v[58:59], v[92:93], v[92:93], v[58:59]
	v_and_b32_e32 v97, 0xffff0000, v38
	v_and_b32_e32 v96, 0xffff0000, v50
	v_pk_fma_f32 v[58:59], v[94:95], v[94:95], v[58:59]
	v_and_b32_e32 v99, 0xffff0000, v39
	v_lshlrev_b32_e32 v39, 16, v39
	v_lshlrev_b32_e32 v38, 16, v51
	v_pk_fma_f32 v[58:59], v[96:97], v[96:97], v[58:59]
	v_and_b32_e32 v98, 0xffff0000, v51
	v_pk_fma_f32 v[38:39], v[38:39], v[38:39], v[58:59]
	v_lshlrev_b32_e32 v61, 16, v40
	v_lshlrev_b32_e32 v60, 16, v52
	v_pk_fma_f32 v[38:39], v[98:99], v[98:99], v[38:39]
	v_and_b32_e32 v101, 0xffff0000, v40
	v_and_b32_e32 v100, 0xffff0000, v52
	v_pk_fma_f32 v[38:39], v[60:61], v[60:61], v[38:39]
	v_lshlrev_b32_e32 v103, 16, v41
	v_lshlrev_b32_e32 v102, 16, v53
	v_pk_fma_f32 v[38:39], v[100:101], v[100:101], v[38:39]
	v_and_b32_e32 v41, 0xffff0000, v41
	v_and_b32_e32 v40, 0xffff0000, v53
	v_pk_fma_f32 v[38:39], v[102:103], v[102:103], v[38:39]
	v_and_b32_e32 v53, 0xffff0000, v46
	v_pk_fma_f32 v[38:39], v[40:41], v[40:41], v[38:39]
	v_lshlrev_b32_e32 v41, 16, v46
	s_waitcnt vmcnt(24)
	v_lshlrev_b32_e32 v40, 16, v54
	v_and_b32_e32 v52, 0xffff0000, v54
	v_pk_fma_f32 v[38:39], v[40:41], v[40:41], v[38:39]
	v_and_b32_e32 v62, 0xffff0000, v48
	v_lshlrev_b32_e32 v63, 16, v48
	v_and_b32_e32 v50, 0xffff0000, v56
	v_lshlrev_b32_e32 v51, 16, v56
	v_pk_fma_f32 v[38:39], v[52:53], v[52:53], v[38:39]
	v_lshlrev_b32_e32 v41, 16, v47
	v_lshlrev_b32_e32 v40, 16, v55
	v_pk_mul_f32 v[62:63], v[62:63], v[62:63]
	v_pk_mul_f32 v[50:51], v[50:51], v[50:51]
	v_and_b32_e32 v47, 0xffff0000, v47
	v_and_b32_e32 v46, 0xffff0000, v55
	v_pk_fma_f32 v[38:39], v[40:41], v[40:41], v[38:39]
	v_mov_b32_e32 v40, v51
	v_pk_fma_f32 v[38:39], v[46:47], v[46:47], v[38:39]
	v_mov_b32_e32 v41, v63
	v_and_b32_e32 v48, 0xffff0000, v49
	v_lshlrev_b32_e32 v49, 16, v49
	v_pk_add_f32 v[38:39], v[40:41], v[38:39]
	v_and_b32_e32 v40, 0xffff0000, v57
	v_lshlrev_b32_e32 v41, 16, v57
	v_pk_mul_f32 v[48:49], v[48:49], v[48:49]
	v_pk_mul_f32 v[40:41], v[40:41], v[40:41]
	v_mov_b32_e32 v51, v62
	v_pk_add_f32 v[38:39], v[50:51], v[38:39]
	v_mov_b32_e32 v46, v41
	v_mov_b32_e32 v47, v49
	v_pk_add_f32 v[38:39], v[46:47], v[38:39]
	v_mov_b32_e32 v41, v48
	v_pk_add_f32 v[46:47], v[40:41], v[38:39]
	ds_bpermute_b32 v49, v1, v47
	ds_bpermute_b32 v48, v1, v46
	s_waitcnt vmcnt(17)
	v_mov_b64_e32 v[38:39], v[134:135]
	v_mov_b64_e32 v[40:41], v[136:137]
	s_waitcnt vmcnt(17)
	v_and_b32_e32 v58, 0xffff0000, v44
	v_lshlrev_b32_e32 v59, 16, v44
	v_and_b32_e32 v44, 0xffff0000, v45
	s_waitcnt lgkmcnt(0)
	v_pk_add_f32 v[46:47], v[46:47], v[48:49]
	ds_bpermute_b32 v49, v201, v47
	ds_bpermute_b32 v48, v201, v46
	v_lshlrev_b32_e32 v45, 16, v45
	v_pk_mul_f32 v[60:61], v[44:45], v[44:45]
	v_lshlrev_b32_e32 v45, 16, v18
	s_waitcnt vmcnt(17)
	v_lshlrev_b32_e32 v44, 16, v26
	s_waitcnt lgkmcnt(0)
	v_pk_add_f32 v[50:51], v[46:47], v[48:49]
	s_waitcnt vmcnt(16)
	v_mov_b64_e32 v[46:47], v[138:139]
	v_mov_b64_e32 v[48:49], v[140:141]
	v_and_b32_e32 v63, 0xffff0000, v18
	v_and_b32_e32 v62, 0xffff0000, v26
	v_pk_mul_f32 v[44:45], v[44:45], v[44:45]
	v_and_b32_e32 v65, 0xffff0000, v19
	v_pk_fma_f32 v[44:45], v[62:63], v[62:63], v[44:45]
	v_lshlrev_b32_e32 v63, 16, v19
	v_lshlrev_b32_e32 v62, 16, v27
	v_and_b32_e32 v64, 0xffff0000, v27
	v_pk_fma_f32 v[44:45], v[62:63], v[62:63], v[44:45]
	v_lshlrev_b32_e32 v63, 16, v20
	v_pk_fma_f32 v[44:45], v[64:65], v[64:65], v[44:45]
	v_lshlrev_b32_e32 v62, 16, v28
	v_and_b32_e32 v65, 0xffff0000, v20
	v_and_b32_e32 v64, 0xffff0000, v28
	v_pk_fma_f32 v[44:45], v[62:63], v[62:63], v[44:45]
	v_lshlrev_b32_e32 v63, 16, v21
	v_pk_fma_f32 v[44:45], v[64:65], v[64:65], v[44:45]
	v_lshlrev_b32_e32 v62, 16, v29
	v_pk_fma_f32 v[44:45], v[62:63], v[62:63], v[44:45]
	v_and_b32_e32 v63, 0xffff0000, v21
	v_and_b32_e32 v62, 0xffff0000, v29
	v_lshlrev_b32_e32 v65, 16, v22
	s_waitcnt vmcnt(16)
	v_lshlrev_b32_e32 v64, 16, v30
	v_pk_fma_f32 v[44:45], v[62:63], v[62:63], v[44:45]
	v_and_b32_e32 v55, 0xffff0000, v22
	v_and_b32_e32 v54, 0xffff0000, v30
	v_pk_fma_f32 v[44:45], v[64:65], v[64:65], v[44:45]
	v_and_b32_e32 v63, 0xffff0000, v23
	v_pk_fma_f32 v[44:45], v[54:55], v[54:55], v[44:45]
	v_lshlrev_b32_e32 v55, 16, v23
	v_lshlrev_b32_e32 v54, 16, v31
	v_and_b32_e32 v62, 0xffff0000, v31
	v_pk_fma_f32 v[44:45], v[54:55], v[54:55], v[44:45]
	v_lshlrev_b32_e32 v55, 16, v24
	v_pk_fma_f32 v[44:45], v[62:63], v[62:63], v[44:45]
	v_lshlrev_b32_e32 v54, 16, v32
	v_and_b32_e32 v63, 0xffff0000, v24
	v_and_b32_e32 v62, 0xffff0000, v32
	v_pk_fma_f32 v[44:45], v[54:55], v[54:55], v[44:45]
	v_lshlrev_b32_e32 v55, 16, v25
	v_pk_fma_f32 v[44:45], v[62:63], v[62:63], v[44:45]
	v_lshlrev_b32_e32 v54, 16, v33
	v_and_b32_e32 v63, 0xffff0000, v25
	v_and_b32_e32 v62, 0xffff0000, v33
	v_pk_fma_f32 v[44:45], v[54:55], v[54:55], v[44:45]
	v_lshlrev_b32_e32 v55, 16, v34
	v_pk_fma_f32 v[44:45], v[62:63], v[62:63], v[44:45]
	v_and_b32_e32 v63, 0xffff0000, v34
	v_lshlrev_b32_e32 v57, 16, v36
	v_pk_mul_f32 v[58:59], v[58:59], v[58:59]
	v_and_b32_e32 v65, 0xffff0000, v43
	ds_bpermute_b32 v53, v220, v51
	ds_bpermute_b32 v52, v220, v50
	v_mov_b64_e32 v[78:79], s[20:21]
	s_lshr_b32 s20, s25, 20
	s_add_i32 s20, s24, s20
	s_ashr_i32 s26, s20, 12
	s_waitcnt lgkmcnt(0)
	v_pk_add_f32 v[50:51], v[50:51], v[52:53]
	ds_bpermute_b32 v53, v221, v51
	ds_bpermute_b32 v52, v221, v50
	s_waitcnt lgkmcnt(0)
	v_pk_add_f32 v[50:51], v[50:51], v[52:53]
	ds_bpermute_b32 v53, v222, v51
	ds_bpermute_b32 v52, v222, v50
	s_waitcnt vmcnt(16)
; __device__ __forceinline__ float bf_lo(unsigned w) { return __uint_as_float(w << 16); }
; __device__ __forceinline__ float bf_hi(unsigned w) { return __uint_as_float(w & 0xffff0000u); }
; __device__ __forceinline__ void phase_nrr(const Frame& F, const Args& a, int l, const bf16_t* XA, const float* g, const float* modl, unsigned char* XN8) {
;     ...
;         for (int i4 = 0; i4 < 2; ++i4) { u32x4 rw[4][4];
; #pragma unroll
;             for (int i = 0; i < 4; ++i)
; #pragma unroll
;                 for (int j = 0; j < 4; ++j) rw[i][j] = *(const u32x4*)(XA + (size_t)(tb + 4 * i4 + i) * D + (j * 64 + lane) * 8);
; #pragma unroll
;             for (int i = 0; i < 4; ++i) { float ss = 0.f;
; #pragma unroll
;                 for (int j = 0; j < 4; ++j)
; #pragma unroll
;                     for (int q = 0; q < 4; ++q) { const float x0 = bf_lo(rw[i][j][q]), x1 = bf_hi(rw[i][j][q]); ss += x0 * x0; ss += x1 * x1; }
;                 rs[4 * i4 + i] = rsqrtf(wave_sum(ss) * (1.f / D) + EPS); } }
	v_lshlrev_b32_e32 v54, 16, v38
	v_and_b32_e32 v62, 0xffff0000, v38
	v_pk_fma_f32 v[44:45], v[54:55], v[54:55], v[44:45]
	v_and_b32_e32 v55, 0xffff0000, v35
	v_pk_fma_f32 v[44:45], v[62:63], v[62:63], v[44:45]
	v_lshlrev_b32_e32 v35, 16, v35
	v_lshlrev_b32_e32 v34, 16, v39
	v_and_b32_e32 v54, 0xffff0000, v39
	v_pk_fma_f32 v[34:35], v[34:35], v[34:35], v[44:45]
	v_lshlrev_b32_e32 v56, 16, v40
	v_pk_fma_f32 v[34:35], v[54:55], v[54:55], v[34:35]
	s_waitcnt lgkmcnt(0)
	v_pk_add_f32 v[50:51], v[50:51], v[52:53]
	s_waitcnt vmcnt(16)
	v_and_b32_e32 v38, 0xffff0000, v48
	v_lshlrev_b32_e32 v39, 16, v48
	v_pk_mul_f32 v[62:63], v[38:39], v[38:39]
	v_and_b32_e32 v39, 0xffff0000, v36
	v_and_b32_e32 v38, 0xffff0000, v40
	v_pk_fma_f32 v[34:35], v[56:57], v[56:57], v[34:35]
	v_and_b32_e32 v36, 0xffff0000, v41
	v_pk_fma_f32 v[34:35], v[38:39], v[38:39], v[34:35]
	v_lshlrev_b32_e32 v39, 16, v37
	v_lshlrev_b32_e32 v38, 16, v41
	v_and_b32_e32 v37, 0xffff0000, v37
	v_pk_fma_f32 v[34:35], v[38:39], v[38:39], v[34:35]
	v_and_b32_e32 v39, 0xffff0000, v42
	v_pk_fma_f32 v[34:35], v[36:37], v[36:37], v[34:35]
	v_lshlrev_b32_e32 v37, 16, v42
	v_lshlrev_b32_e32 v36, 16, v46
	v_and_b32_e32 v38, 0xffff0000, v46
	v_pk_fma_f32 v[34:35], v[36:37], v[36:37], v[34:35]
	v_lshlrev_b32_e32 v57, 16, v43
	v_pk_fma_f32 v[54:55], v[38:39], v[38:39], v[34:35]
	v_lshlrev_b32_e32 v56, 16, v47
	v_and_b32_e32 v64, 0xffff0000, v47
	v_pk_fma_f32 v[46:47], v[56:57], v[56:57], v[54:55]
	v_mov_b32_e32 v54, v63
	v_pk_fma_f32 v[46:47], v[64:65], v[64:65], v[46:47]
	v_mov_b32_e32 v55, v59
	v_and_b32_e32 v48, 0xffff0000, v49
	v_lshlrev_b32_e32 v49, 16, v49
	v_pk_add_f32 v[46:47], v[54:55], v[46:47]
	v_pk_mul_f32 v[48:49], v[48:49], v[48:49]
	v_mov_b32_e32 v63, v58
	s_waitcnt vmcnt(15)
	v_mov_b64_e32 v[34:35], v[142:143]
	v_mov_b64_e32 v[36:37], v[144:145]
	s_waitcnt vmcnt(14)
	v_mov_b64_e32 v[38:39], v[146:147]
	v_mov_b64_e32 v[40:41], v[148:149]
	s_waitcnt vmcnt(13)
	v_mov_b64_e32 v[80:81], v[150:151]
	v_mov_b64_e32 v[82:83], v[152:153]
	s_waitcnt vmcnt(12)
	v_mov_b64_e32 v[84:85], v[154:155]
	v_mov_b64_e32 v[86:87], v[156:157]
	s_waitcnt vmcnt(11)
	v_mov_b64_e32 v[42:43], v[158:159]
	v_mov_b64_e32 v[44:45], v[160:161]
	v_pk_add_f32 v[46:47], v[62:63], v[46:47]
	v_mov_b32_e32 v54, v49
	v_mov_b32_e32 v55, v61
	v_pk_add_f32 v[46:47], v[54:55], v[46:47]
	v_mov_b32_e32 v49, v60
	v_pk_add_f32 v[46:47], v[48:49], v[46:47]
	ds_bpermute_b32 v49, v1, v47
	ds_bpermute_b32 v48, v1, v46
	s_waitcnt vmcnt(10)
	v_mov_b64_e32 v[88:89], v[162:163]
	v_mov_b64_e32 v[90:91], v[164:165]
	s_waitcnt vmcnt(9)
	v_mov_b64_e32 v[92:93], v[166:167]
	v_mov_b64_e32 v[94:95], v[168:169]
	ds_bpermute_b32 v53, v223, v51
	ds_bpermute_b32 v52, v223, v50
	s_waitcnt lgkmcnt(2)
	v_pk_add_f32 v[54:55], v[46:47], v[48:49]
	s_waitcnt vmcnt(8)
	v_mov_b64_e32 v[46:47], v[170:171]
	v_mov_b64_e32 v[48:49], v[172:173]
	ds_bpermute_b32 v57, v201, v55
	ds_bpermute_b32 v56, v201, v54
	s_waitcnt lgkmcnt(2)
	v_pk_add_f32 v[50:51], v[50:51], v[52:53]
	s_waitcnt lgkmcnt(0)
	v_pk_add_f32 v[52:53], v[54:55], v[56:57]
	ds_bpermute_b32 v55, v220, v53
	ds_bpermute_b32 v54, v220, v52
	v_pk_fma_f32 v[50:51], v[50:51], s[52:53], v[78:79] op_sel_hi:[1,0,0]
	s_waitcnt lgkmcnt(0)
	v_pk_add_f32 v[52:53], v[52:53], v[54:55]
	ds_bpermute_b32 v55, v221, v53
	ds_bpermute_b32 v54, v221, v52
	v_mul_f32_e32 v56, 0x4b800000, v51
	v_cmp_gt_f32_e32 vcc, s83, v51
	v_cmp_gt_f32_e64 s[20:21], s83, v50
	s_waitcnt lgkmcnt(0)
	v_pk_add_f32 v[52:53], v[52:53], v[54:55]
	v_cndmask_b32_e32 v51, v51, v56, vcc
	v_rsq_f32_e32 v51, v51
	ds_bpermute_b32 v55, v222, v53
	ds_bpermute_b32 v54, v222, v52
	v_mul_f32_e32 v56, 0x45800000, v51
	v_cndmask_b32_e32 v246, v51, v56, vcc
	v_mul_f32_e32 v51, 0x4b800000, v50
	v_cndmask_b32_e64 v112, v50, v51, s[20:21]
	s_waitcnt lgkmcnt(0)
	v_pk_add_f32 v[96:97], v[52:53], v[54:55]
	s_waitcnt vmcnt(7)
	v_mov_b64_e32 v[50:51], v[174:175]
	v_mov_b64_e32 v[52:53], v[176:177]
	s_waitcnt vmcnt(6)
	v_mov_b64_e32 v[54:55], v[178:179]
	v_mov_b64_e32 v[56:57], v[180:181]
	s_waitcnt vmcnt(5)
	v_mov_b64_e32 v[70:71], v[182:183]
	v_mov_b64_e32 v[72:73], v[184:185]
	s_waitcnt vmcnt(4)
	v_mov_b64_e32 v[66:67], v[186:187]
	v_mov_b64_e32 v[68:69], v[188:189]
	s_waitcnt vmcnt(3)
	v_mov_b64_e32 v[58:59], v[190:191]
	v_mov_b64_e32 v[60:61], v[192:193]
	s_waitcnt vmcnt(2)
	v_mov_b64_e32 v[62:63], v[114:115]
	v_mov_b64_e32 v[64:65], v[116:117]
	s_waitcnt vmcnt(1)
	v_mov_b64_e32 v[74:75], v[118:119]
	v_mov_b64_e32 v[76:77], v[120:121]
	ds_bpermute_b32 v99, v223, v97
	ds_bpermute_b32 v98, v223, v96
	s_waitcnt vmcnt(1)
	v_lshlrev_b32_e32 v107, 16, v34
	v_and_b32_e32 v109, 0xffff0000, v34
	v_and_b32_e32 v111, 0xffff0000, v35
	s_waitcnt vmcnt(1)
	v_and_b32_e32 v101, 0xffff0000, v38
	s_waitcnt vmcnt(1)
	v_lshlrev_b32_e32 v106, 16, v42
	v_and_b32_e32 v108, 0xffff0000, v42
	v_pk_mul_f32 v[106:107], v[106:107], v[106:107]
	v_and_b32_e32 v110, 0xffff0000, v43
	v_pk_fma_f32 v[106:107], v[108:109], v[108:109], v[106:107]
	v_lshlrev_b32_e32 v109, 16, v35
	v_lshlrev_b32_e32 v108, 16, v43
	v_pk_fma_f32 v[106:107], v[108:109], v[108:109], v[106:107]
	v_lshlrev_b32_e32 v109, 16, v36
	v_pk_fma_f32 v[106:107], v[110:111], v[110:111], v[106:107]
	v_lshlrev_b32_e32 v108, 16, v44
	v_and_b32_e32 v111, 0xffff0000, v36
	v_and_b32_e32 v110, 0xffff0000, v44
	v_pk_fma_f32 v[106:107], v[108:109], v[108:109], v[106:107]
	v_lshlrev_b32_e32 v109, 16, v37
	v_pk_fma_f32 v[106:107], v[110:111], v[110:111], v[106:107]
	v_lshlrev_b32_e32 v108, 16, v45
	v_pk_fma_f32 v[106:107], v[108:109], v[108:109], v[106:107]
	v_and_b32_e32 v109, 0xffff0000, v37
	v_and_b32_e32 v108, 0xffff0000, v45
	v_lshlrev_b32_e32 v111, 16, v38
	s_waitcnt vmcnt(1)
; __device__ __forceinline__ float bf_lo(unsigned w) { return __uint_as_float(w << 16); }
; __device__ __forceinline__ float bf_hi(unsigned w) { return __uint_as_float(w & 0xffff0000u); }
; __device__ __forceinline__ void phase_nrr(const Frame& F, const Args& a, int l, const bf16_t* XA, const float* g, const float* modl, unsigned char* XN8) {
;     ...
;         for (int i4 = 0; i4 < 2; ++i4) { u32x4 rw[4][4];
; #pragma unroll
;             for (int i = 0; i < 4; ++i)
; #pragma unroll
;                 for (int j = 0; j < 4; ++j) rw[i][j] = *(const u32x4*)(XA + (size_t)(tb + 4 * i4 + i) * D + (j * 64 + lane) * 8);
; #pragma unroll
;             for (int i = 0; i < 4; ++i) { float ss = 0.f;
; #pragma unroll
;                 for (int j = 0; j < 4; ++j)
; #pragma unroll
;                     for (int q = 0; q < 4; ++q) { const float x0 = bf_lo(rw[i][j][q]), x1 = bf_hi(rw[i][j][q]); ss += x0 * x0; ss += x1 * x1; }
;                 rs[4 * i4 + i] = rsqrtf(wave_sum(ss) * (1.f / D) + EPS); } }
	v_lshlrev_b32_e32 v110, 16, v46
	v_pk_fma_f32 v[106:107], v[108:109], v[108:109], v[106:107]
	v_and_b32_e32 v100, 0xffff0000, v46
	v_pk_fma_f32 v[106:107], v[110:111], v[110:111], v[106:107]
	v_and_b32_e32 v109, 0xffff0000, v39
	v_pk_fma_f32 v[100:101], v[100:101], v[100:101], v[106:107]
	v_lshlrev_b32_e32 v107, 16, v39
	v_lshlrev_b32_e32 v106, 16, v47
	v_and_b32_e32 v108, 0xffff0000, v47
	v_pk_fma_f32 v[100:101], v[106:107], v[106:107], v[100:101]
	v_lshlrev_b32_e32 v107, 16, v40
	v_pk_fma_f32 v[100:101], v[108:109], v[108:109], v[100:101]
	v_lshlrev_b32_e32 v106, 16, v48
	v_and_b32_e32 v109, 0xffff0000, v40
	v_and_b32_e32 v108, 0xffff0000, v48
	v_pk_fma_f32 v[100:101], v[106:107], v[106:107], v[100:101]
	v_lshlrev_b32_e32 v107, 16, v41
	v_pk_fma_f32 v[100:101], v[108:109], v[108:109], v[100:101]
	v_lshlrev_b32_e32 v106, 16, v49
	v_and_b32_e32 v109, 0xffff0000, v41
	v_and_b32_e32 v108, 0xffff0000, v49
	v_pk_fma_f32 v[100:101], v[106:107], v[106:107], v[100:101]
	v_lshlrev_b32_e32 v107, 16, v80
	v_pk_fma_f32 v[100:101], v[108:109], v[108:109], v[100:101]
	v_lshlrev_b32_e32 v106, 16, v88
	v_and_b32_e32 v109, 0xffff0000, v80
	v_and_b32_e32 v108, 0xffff0000, v88
	v_pk_fma_f32 v[100:101], v[106:107], v[106:107], v[100:101]
	v_and_b32_e32 v107, 0xffff0000, v81
	v_pk_fma_f32 v[100:101], v[108:109], v[108:109], v[100:101]
	v_lshlrev_b32_e32 v81, 16, v81
	v_lshlrev_b32_e32 v80, 16, v89
	v_and_b32_e32 v106, 0xffff0000, v89
	v_pk_fma_f32 v[80:81], v[80:81], v[80:81], v[100:101]
	v_lshlrev_b32_e32 v103, 16, v82
	v_lshlrev_b32_e32 v102, 16, v90
	v_pk_fma_f32 v[80:81], v[106:107], v[106:107], v[80:81]
	v_and_b32_e32 v101, 0xffff0000, v82
	v_and_b32_e32 v100, 0xffff0000, v90
	v_pk_fma_f32 v[80:81], v[102:103], v[102:103], v[80:81]
	v_and_b32_e32 v82, 0xffff0000, v91
	v_pk_fma_f32 v[80:81], v[100:101], v[100:101], v[80:81]
	v_lshlrev_b32_e32 v101, 16, v83
	v_lshlrev_b32_e32 v100, 16, v91
	v_and_b32_e32 v83, 0xffff0000, v83
	v_pk_fma_f32 v[80:81], v[100:101], v[100:101], v[80:81]
	v_and_b32_e32 v91, 0xffff0000, v84
	v_pk_fma_f32 v[80:81], v[82:83], v[82:83], v[80:81]
	v_lshlrev_b32_e32 v83, 16, v84
	v_lshlrev_b32_e32 v82, 16, v92
	v_and_b32_e32 v90, 0xffff0000, v92
	v_pk_fma_f32 v[80:81], v[82:83], v[82:83], v[80:81]
	v_and_b32_e32 v104, 0xffff0000, v86
	v_lshlrev_b32_e32 v105, 16, v86
	v_and_b32_e32 v88, 0xffff0000, v94
	v_lshlrev_b32_e32 v89, 16, v94
	v_pk_fma_f32 v[80:81], v[90:91], v[90:91], v[80:81]
	v_lshlrev_b32_e32 v83, 16, v85
	v_lshlrev_b32_e32 v82, 16, v93
	v_pk_mul_f32 v[104:105], v[104:105], v[104:105]
	v_pk_mul_f32 v[88:89], v[88:89], v[88:89]
	v_and_b32_e32 v85, 0xffff0000, v85
	v_and_b32_e32 v84, 0xffff0000, v93
	v_pk_fma_f32 v[80:81], v[82:83], v[82:83], v[80:81]
	v_mov_b32_e32 v82, v89
	v_pk_fma_f32 v[80:81], v[84:85], v[84:85], v[80:81]
	v_mov_b32_e32 v83, v105
	v_and_b32_e32 v86, 0xffff0000, v87
	v_lshlrev_b32_e32 v87, 16, v87
	v_pk_add_f32 v[80:81], v[82:83], v[80:81]
	v_and_b32_e32 v82, 0xffff0000, v95
	v_lshlrev_b32_e32 v83, 16, v95
	v_pk_mul_f32 v[86:87], v[86:87], v[86:87]
	v_pk_mul_f32 v[82:83], v[82:83], v[82:83]
	v_mov_b32_e32 v89, v104
	v_pk_add_f32 v[80:81], v[88:89], v[80:81]
	v_mov_b32_e32 v84, v83
	v_mov_b32_e32 v85, v87
	v_pk_add_f32 v[80:81], v[84:85], v[80:81]
	v_mov_b32_e32 v83, v86
	v_pk_add_f32 v[80:81], v[82:83], v[80:81]
	ds_bpermute_b32 v83, v1, v81
	ds_bpermute_b32 v82, v1, v80
	s_waitcnt lgkmcnt(2)
	v_pk_add_f32 v[84:85], v[96:97], v[98:99]
	s_waitcnt vmcnt(1)
	v_lshlrev_b32_e32 v97, 16, v50
	s_waitcnt vmcnt(1)
	v_lshlrev_b32_e32 v96, 16, v58
	v_and_b32_e32 v99, 0xffff0000, v50
	s_waitcnt lgkmcnt(0)
	v_pk_add_f32 v[86:87], v[80:81], v[82:83]
	s_waitcnt vmcnt(0)
	v_mov_b64_e32 v[80:81], v[126:127]
	v_mov_b64_e32 v[82:83], v[128:129]
	v_and_b32_e32 v98, 0xffff0000, v58
	v_pk_mul_f32 v[96:97], v[96:97], v[96:97]
	v_and_b32_e32 v101, 0xffff0000, v51
	v_pk_fma_f32 v[96:97], v[98:99], v[98:99], v[96:97]
	v_lshlrev_b32_e32 v99, 16, v51
	v_lshlrev_b32_e32 v98, 16, v59
	v_and_b32_e32 v100, 0xffff0000, v59
	v_pk_fma_f32 v[96:97], v[98:99], v[98:99], v[96:97]
	v_rsq_f32_e32 v90, v112
	v_pk_fma_f32 v[96:97], v[100:101], v[100:101], v[96:97]
	v_lshlrev_b32_e32 v99, 16, v52
	v_lshlrev_b32_e32 v98, 16, v60
	v_and_b32_e32 v101, 0xffff0000, v52
	v_and_b32_e32 v100, 0xffff0000, v60
	v_pk_fma_f32 v[96:97], v[98:99], v[98:99], v[96:97]
	v_pk_fma_f32 v[84:85], v[84:85], s[52:53], v[78:79] op_sel_hi:[1,0,0]
	v_pk_fma_f32 v[96:97], v[100:101], v[100:101], v[96:97]
	v_lshlrev_b32_e32 v99, 16, v53
	v_lshlrev_b32_e32 v98, 16, v61
	v_mul_f32_e32 v91, 0x4b800000, v85
	v_cmp_gt_f32_e32 vcc, s83, v85
	v_pk_fma_f32 v[96:97], v[98:99], v[98:99], v[96:97]
	v_and_b32_e32 v99, 0xffff0000, v53
	v_and_b32_e32 v98, 0xffff0000, v61
	v_cndmask_b32_e32 v85, v85, v91, vcc
	v_mul_f32_e32 v91, 0x45800000, v90
	v_lshlrev_b32_e32 v101, 16, v54
	s_waitcnt vmcnt(2)
	v_lshlrev_b32_e32 v100, 16, v62
	v_pk_fma_f32 v[96:97], v[98:99], v[98:99], v[96:97]
	v_cndmask_b32_e64 v247, v90, v91, s[20:21]
	v_and_b32_e32 v91, 0xffff0000, v54
	v_and_b32_e32 v90, 0xffff0000, v62
	v_pk_fma_f32 v[96:97], v[100:101], v[100:101], v[96:97]
	v_and_b32_e32 v99, 0xffff0000, v55
	v_pk_fma_f32 v[90:91], v[90:91], v[90:91], v[96:97]
	v_lshlrev_b32_e32 v97, 16, v55
	v_lshlrev_b32_e32 v96, 16, v63
	v_and_b32_e32 v98, 0xffff0000, v63
	v_pk_fma_f32 v[90:91], v[96:97], v[96:97], v[90:91]
	v_lshlrev_b32_e32 v97, 16, v56
	v_pk_fma_f32 v[90:91], v[98:99], v[98:99], v[90:91]
	v_lshlrev_b32_e32 v96, 16, v64
	v_and_b32_e32 v99, 0xffff0000, v56
	v_and_b32_e32 v98, 0xffff0000, v64
	v_pk_fma_f32 v[90:91], v[96:97], v[96:97], v[90:91]
	v_lshlrev_b32_e32 v97, 16, v57
	v_pk_fma_f32 v[90:91], v[98:99], v[98:99], v[90:91]
	v_lshlrev_b32_e32 v96, 16, v65
	v_and_b32_e32 v99, 0xffff0000, v57
	v_and_b32_e32 v98, 0xffff0000, v65
	v_pk_fma_f32 v[90:91], v[96:97], v[96:97], v[90:91]
	v_lshlrev_b32_e32 v97, 16, v70
	v_pk_fma_f32 v[90:91], v[98:99], v[98:99], v[90:91]
	s_waitcnt vmcnt(1)
; __device__ __forceinline__ float bf_lo(unsigned w) { return __uint_as_float(w << 16); }
; __device__ __forceinline__ float bf_hi(unsigned w) { return __uint_as_float(w & 0xffff0000u); }
; __device__ __forceinline__ void phase_nrr(const Frame& F, const Args& a, int l, const bf16_t* XA, const float* g, const float* modl, unsigned char* XN8) {
;     ...
;             for (int i = 0; i < 4; ++i) { float ss = 0.f;
; #pragma unroll
;                 for (int j = 0; j < 4; ++j)
; #pragma unroll
;                     for (int q = 0; q < 4; ++q) { const float x0 = bf_lo(rw[i][j][q]), x1 = bf_hi(rw[i][j][q]); ss += x0 * x0; ss += x1 * x1; }
;                 rs[4 * i4 + i] = rsqrtf(wave_sum(ss) * (1.f / D) + EPS); } }
;         f32x4 acc[4] = {{0.f, 0.f, 0.f, 0.f}, {0.f, 0.f, 0.f, 0.f}, {0.f, 0.f, 0.f, 0.f}, {0.f, 0.f, 0.f, 0.f}};
;         u32x4 raw[8][2];
; #pragma unroll
;         for (int i = 0; i < 8; ++i)
; #pragma unroll
;             for (int jj = 0; jj < 2; ++jj) raw[i][jj] = __builtin_nontemporal_load((const u32x4*)(XA + (size_t)(tb + i) * D + (jj * 64 + lane) * 8));
; #pragma unroll 1
;         for (int h = 0; h < 2; ++h) {
;             const bf16_t* wrow = Wr + (size_t)(16 * eb + fr) * D + h * 1024 + 512 * kq + 8 * fq;
;             bf16x8 bv[16];
; #pragma unroll
;             for (int kb = 0; kb < 16; ++kb) bv[kb] = *(const bf16x8*)(wrow + 32 * kb);
;             float gs[2][8], shv[2][8];
; #pragma unroll
;             for (int jj = 0; jj < 2; ++jj) { const int d = ((2 * h + jj) * 64 + lane) * 8; const float* sh = modl + (size_t)b * MODW + 3 * D; const float* sc = modl + (size_t)b * MODW + 4 * D;
	v_lshlrev_b32_e32 v96, 16, v74
	v_and_b32_e32 v99, 0xffff0000, v70
	v_and_b32_e32 v98, 0xffff0000, v74
	v_pk_fma_f32 v[90:91], v[96:97], v[96:97], v[90:91]
	v_and_b32_e32 v97, 0xffff0000, v71
	v_pk_fma_f32 v[90:91], v[98:99], v[98:99], v[90:91]
	v_lshlrev_b32_e32 v71, 16, v71
	v_lshlrev_b32_e32 v70, 16, v75
	v_and_b32_e32 v96, 0xffff0000, v75
	v_pk_fma_f32 v[70:71], v[70:71], v[70:71], v[90:91]
	v_lshlrev_b32_e32 v93, 16, v72
	v_lshlrev_b32_e32 v92, 16, v76
	v_pk_fma_f32 v[70:71], v[96:97], v[96:97], v[70:71]
	v_and_b32_e32 v91, 0xffff0000, v72
	v_and_b32_e32 v90, 0xffff0000, v76
	v_pk_fma_f32 v[70:71], v[92:93], v[92:93], v[70:71]
	v_and_b32_e32 v72, 0xffff0000, v77
	v_pk_fma_f32 v[70:71], v[90:91], v[90:91], v[70:71]
	v_lshlrev_b32_e32 v91, 16, v73
	v_lshlrev_b32_e32 v90, 16, v77
	v_and_b32_e32 v73, 0xffff0000, v73
	v_pk_fma_f32 v[70:71], v[90:91], v[90:91], v[70:71]
	v_and_b32_e32 v77, 0xffff0000, v66
	v_pk_fma_f32 v[70:71], v[72:73], v[72:73], v[70:71]
	v_lshlrev_b32_e32 v73, 16, v66
	v_and_b32_e32 v94, 0xffff0000, v68
	s_waitcnt vmcnt(0)
	v_lshlrev_b32_e32 v72, 16, v80
	v_and_b32_e32 v76, 0xffff0000, v80
	v_pk_fma_f32 v[70:71], v[72:73], v[72:73], v[70:71]
	v_lshlrev_b32_e32 v95, 16, v68
	v_and_b32_e32 v74, 0xffff0000, v82
	v_lshlrev_b32_e32 v75, 16, v82
	v_pk_fma_f32 v[70:71], v[76:77], v[76:77], v[70:71]
	v_lshlrev_b32_e32 v73, 16, v67
	v_lshlrev_b32_e32 v72, 16, v81
	v_pk_mul_f32 v[94:95], v[94:95], v[94:95]
	v_pk_mul_f32 v[74:75], v[74:75], v[74:75]
	v_and_b32_e32 v67, 0xffff0000, v67
	v_and_b32_e32 v66, 0xffff0000, v81
	v_pk_fma_f32 v[70:71], v[72:73], v[72:73], v[70:71]
	v_and_b32_e32 v68, 0xffff0000, v69
	v_pk_fma_f32 v[66:67], v[66:67], v[66:67], v[70:71]
	v_mov_b32_e32 v70, v75
	v_mov_b32_e32 v71, v95
	v_lshlrev_b32_e32 v69, 16, v69
	v_pk_add_f32 v[66:67], v[70:71], v[66:67]
	v_and_b32_e32 v70, 0xffff0000, v83
	v_lshlrev_b32_e32 v71, 16, v83
	v_pk_mul_f32 v[68:69], v[68:69], v[68:69]
	v_pk_mul_f32 v[70:71], v[70:71], v[70:71]
	v_mov_b32_e32 v75, v94
	v_pk_add_f32 v[66:67], v[74:75], v[66:67]
	v_mov_b32_e32 v72, v71
	v_mov_b32_e32 v73, v69
	v_pk_add_f32 v[66:67], v[72:73], v[66:67]
	v_mov_b32_e32 v71, v68
	ds_bpermute_b32 v89, v201, v87
	ds_bpermute_b32 v88, v201, v86
	v_pk_add_f32 v[66:67], v[70:71], v[66:67]
	ds_bpermute_b32 v69, v1, v67
	ds_bpermute_b32 v68, v1, v66
	v_rsq_f32_e32 v85, v85
	s_waitcnt lgkmcnt(2)
	v_pk_add_f32 v[86:87], v[86:87], v[88:89]
	ds_bpermute_b32 v89, v220, v87
	ds_bpermute_b32 v88, v220, v86
	s_waitcnt lgkmcnt(2)
	v_pk_add_f32 v[66:67], v[66:67], v[68:69]
	ds_bpermute_b32 v69, v201, v67
	ds_bpermute_b32 v68, v201, v66
	v_mul_f32_e32 v102, 0x45800000, v85
	s_waitcnt lgkmcnt(2)
	v_pk_add_f32 v[86:87], v[86:87], v[88:89]
	ds_bpermute_b32 v89, v221, v87
	ds_bpermute_b32 v88, v221, v86
	s_waitcnt lgkmcnt(2)
	v_pk_add_f32 v[66:67], v[66:67], v[68:69]
	ds_bpermute_b32 v69, v220, v67
	ds_bpermute_b32 v68, v220, v66
	v_cndmask_b32_e32 v248, v85, v102, vcc
	s_waitcnt lgkmcnt(2)
	v_pk_add_f32 v[70:71], v[86:87], v[88:89]
	ds_bpermute_b32 v73, v222, v71
	ds_bpermute_b32 v72, v222, v70
	s_waitcnt lgkmcnt(2)
	v_pk_add_f32 v[66:67], v[66:67], v[68:69]
	ds_bpermute_b32 v69, v221, v67
	ds_bpermute_b32 v68, v221, v66
	v_mul_f32_e32 v103, 0x4b800000, v84
	s_waitcnt lgkmcnt(2)
	v_pk_add_f32 v[70:71], v[70:71], v[72:73]
	ds_bpermute_b32 v73, v223, v71
	ds_bpermute_b32 v72, v223, v70
	s_waitcnt lgkmcnt(2)
	v_pk_add_f32 v[66:67], v[66:67], v[68:69]
	ds_bpermute_b32 v69, v222, v67
	ds_bpermute_b32 v68, v222, v66
	v_cmp_gt_f32_e64 s[20:21], s83, v84
	s_waitcnt lgkmcnt(2)
	v_pk_add_f32 v[70:71], v[70:71], v[72:73]
	v_mov_b32_e32 v110, 0
	v_pk_fma_f32 v[70:71], v[70:71], s[52:53], v[78:79] op_sel_hi:[1,0,0]
	s_waitcnt lgkmcnt(0)
	v_pk_add_f32 v[66:67], v[66:67], v[68:69]
	v_mul_f32_e32 v72, 0x4b800000, v71
	v_cmp_gt_f32_e32 vcc, s83, v71
	ds_bpermute_b32 v69, v223, v67
	ds_bpermute_b32 v68, v223, v66
	v_cndmask_b32_e32 v71, v71, v72, vcc
	v_cndmask_b32_e64 v74, v84, v103, s[20:21]
	v_rsq_f32_e32 v71, v71
	v_rsq_f32_e32 v74, v74
	v_mul_f32_e32 v72, 0x4b800000, v70
	v_cmp_gt_f32_e64 s[22:23], s83, v70
	s_waitcnt lgkmcnt(0)
	v_pk_add_f32 v[66:67], v[66:67], v[68:69]
	v_mul_f32_e32 v75, 0x45800000, v74
	v_cndmask_b32_e64 v70, v70, v72, s[22:23]
	v_mul_f32_e32 v72, 0x45800000, v71
	v_pk_fma_f32 v[66:67], v[66:67], s[52:53], v[78:79] op_sel_hi:[1,0,0]
	v_cndmask_b32_e32 v250, v71, v72, vcc
	v_mul_f32_e32 v68, 0x4b800000, v67
	v_cmp_gt_f32_e32 vcc, s83, v67
	v_cndmask_b32_e64 v249, v74, v75, s[20:21]
	v_cmp_gt_f32_e64 s[20:21], s83, v66
	v_cndmask_b32_e32 v67, v67, v68, vcc
	v_mul_f32_e32 v68, 0x4b800000, v66
	v_rsq_f32_e32 v67, v67
	v_cndmask_b32_e64 v66, v66, v68, s[20:21]
	v_rsq_f32_e32 v66, v66
	v_rsq_f32_e32 v70, v70
	v_mul_f32_e32 v68, 0x45800000, v67
	v_cndmask_b32_e32 v252, v67, v68, vcc
	v_mul_f32_e32 v67, 0x45800000, v66
	v_mul_f32_e32 v71, 0x45800000, v70
	v_cndmask_b32_e64 v253, v66, v67, s[20:21]
	s_mul_hi_i32 s20, s26, 0xc000
	s_mul_i32 s26, s26, 0xc000
	v_cndmask_b32_e64 v251, v70, v71, s[22:23]
	s_add_u32 s22, s53, s26
	s_addc_u32 s23, s68, s20
	s_add_u32 s20, s22, 0x6000
	s_addc_u32 s21, s23, 0
	s_add_u32 s22, s22, 0x8000
	s_addc_u32 s23, s23, 0
	s_lshl_b64 s[26:27], s[24:25], 11
	s_add_u32 s26, s69, s26
	s_addc_u32 s27, s70, s27
	s_lshl_b64 s[28:29], s[56:57], 11
	s_add_u32 s28, s69, s28
	s_addc_u32 s29, s70, s29
	s_lshl_b64 s[30:31], s[54:55], 11
	s_add_u32 s30, s69, s30
	s_addc_u32 s31, s70, s31
	s_lshl_b64 s[34:35], s[4:5], 11
	s_add_u32 s34, s69, s34
	s_addc_u32 s35, s70, s35
	s_lshl_b64 s[36:37], s[2:3], 11
	s_add_u32 s36, s69, s36
	s_addc_u32 s37, s70, s37
	s_lshl_b64 s[40:41], s[40:41], 11
	s_add_u32 s40, s69, s40
	s_addc_u32 s41, s70, s41
	s_lshl_b64 s[58:59], s[58:59], 11
	s_add_u32 s58, s69, s58
	s_addc_u32 s59, s70, s59
	s_lshl_b64 s[60:61], s[60:61], 11
	s_add_u32 s60, s69, s60
	s_addc_u32 s61, s70, s61
	v_mov_b32_e32 v111, v110
	v_mov_b32_e32 v112, v110
	v_mov_b32_e32 v113, v110
	v_mov_b32_e32 v118, v110
	v_mov_b32_e32 v119, v110
	v_mov_b32_e32 v120, v110
	v_mov_b32_e32 v121, v110
	v_mov_b32_e32 v126, v110
	v_mov_b32_e32 v127, v110
	v_mov_b32_e32 v128, v110
	v_mov_b32_e32 v129, v110
	v_mov_b32_e32 v130, v110
	v_mov_b32_e32 v131, v110
	v_mov_b32_e32 v132, v110
	v_mov_b32_e32 v133, v110
	s_branch .LBB0_1304
